# combined version plus gMLP epilogue de-serialisation: second bias load issued with the first, store-draining vmcnt(0) removed
# speedup vs baseline: 1.0071x; 1.0071x over previous
; __device__ __forceinline__ void gmlp_unit(Ctx& C, int l, int uidx) {
;     ...
;     const int ck = uidx >> 1, hf = uidx & 1, row0 = 128 * ck;
;     const bf16* Z = WSP(bf16, WS_Z);
;     const int gl = C.wave >> 1, ph = C.wave & 1, g = 4 * hf + gl, r32 = C.lane & 31, h = C.lane >> 5;
;     bf16x8 Wf[2][8]; u32x2 upre[2][2][4];
;     { const bf16* wsb = WSP(bf16, WS_GWSB) + ((size_t)(l * 8 + g) * 128 + 64 * ph + r32) * 128 + 8 * h;
; #pragma unroll
;       for (int pb = 0; pb < 2; ++pb)
; #pragma unroll
;           for (int s = 0; s < 8; ++s) Wf[pb][s] = *(const bf16x8*)(wsb + (size_t)(32 * pb) * 128 + 16 * s);
; #pragma unroll
;       for (int pb = 0; pb < 2; ++pb) { const bf16* up = Z + (size_t)(row0 + 64 * ph + 32 * pb + r32) * INW + 2816 + 64 * g + 4 * h;
; #pragma unroll
;           for (int cb = 0; cb < 2; ++cb)
; #pragma unroll
;               for (int rg = 0; rg < 4; ++rg) upre[pb][cb][rg] = *(const u32x2*)(up + 32 * cb + 8 * rg); } }
;     __syncthreads();
;     {
;         const int tok = C.tid >> 2, part = C.tid & 3;
;         const bf16* zp = Z + (size_t)(row0 + tok) * INW + 3328 + 128 * part;
;         const bf16* zq = Z + (size_t)(row0 + tok) * INW + 3328 + 256 * hf + 64 * part;
;         u32x4 r1[16], r2[8];
; #pragma unroll
;         for (int c8 = 0; c8 < 16; ++c8) r1[c8] = *(const u32x4*)(zp + 8 * c8);
; #pragma unroll
;         for (int c8 = 0; c8 < 8; ++c8) r2[c8] = *(const u32x4*)(zq + 8 * c8);
.LBB0_495:
	s_andn2_b64 vcc, exec, s[6:7]
	s_cbranch_vccnz .LBB0_497
	s_and_b32 s6, s43, 1
	s_ashr_i32 s19, s51, 7
	s_lshl_b32 s8, s6, 2
	s_add_i32 s14, s19, s8
	s_ashr_i32 s15, s14, 31
	s_lshl_b64 s[8:9], s[14:15], 7
	s_and_b32 s15, s51, 64
	v_and_b32_e32 v159, 31, v178
	s_or_b32 s8, s8, s15
	v_or_b32_e32 v4, s8, v159
	v_mov_b32_e32 v5, s9
	v_lshrrev_b32_e32 v6, 5, v162
	v_lshlrev_b64 v[4:5], 8, v[4:5]
	v_lshl_add_u64 v[4:5], s[54:55], 0, v[4:5]
	v_lshlrev_b32_e32 v156, 4, v6
	v_mov_b32_e32 v157, v3
	v_lshl_add_u64 v[8:9], v[4:5], 0, v[156:157]
	s_mov_b64 s[8:9], 0x380000
	s_lshl_b32 s7, s43, 6
	v_lshl_add_u64 v[10:11], v[8:9], 0, s[8:9]
	s_mov_b32 s8, 0x380000
	s_addk_i32 s7, 0x3c00
	v_add_co_u32_e32 v4, vcc, s8, v8
	s_mov_b32 s8, 0x382000
	s_nop 0
	v_addc_co_u32_e32 v5, vcc, 0, v9, vcc
	s_and_b32 s18, s7, 0x7f80
	v_add_co_u32_e32 v12, vcc, s8, v8
	s_add_u32 s8, s54, 0x36000000
	s_nop 0
	v_addc_co_u32_e32 v13, vcc, 0, v9, vcc
	s_addc_u32 s9, s55, 0
	s_or_b32 s7, s18, s15
	v_lshlrev_b32_e32 v2, 3, v6
	global_load_dwordx4 v[116:119], v[10:11], off offset:32
	global_load_dwordx4 v[104:107], v[10:11], off offset:64
	global_load_dwordx4 v[100:103], v[10:11], off offset:96
	global_load_dwordx4 v[88:91], v[10:11], off offset:128
	global_load_dwordx4 v[84:87], v[10:11], off offset:160
	global_load_dwordx4 v[76:79], v[10:11], off offset:192
	s_nop 0
	global_load_dwordx4 v[4:7], v[4:5], off
	s_nop 0
	global_load_dwordx4 v[72:75], v[10:11], off offset:224
	s_nop 0
	global_load_dwordx4 v[8:11], v[12:13], off
	global_load_dwordx4 v[120:123], v[12:13], off offset:32
	global_load_dwordx4 v[112:115], v[12:13], off offset:64
	global_load_dwordx4 v[108:111], v[12:13], off offset:96
	global_load_dwordx4 v[96:99], v[12:13], off offset:128
	global_load_dwordx4 v[92:95], v[12:13], off offset:160
	global_load_dwordx4 v[80:83], v[12:13], off offset:192
	global_load_dwordx4 v[68:71], v[12:13], off offset:224
	v_or_b32_e32 v12, s7, v159
	s_lshl_b32 s10, s14, 6
	v_mul_u32_u24_e32 v12, 0xf00, v12
	s_ashr_i32 s11, s10, 31
	v_lshlrev_b32_e32 v12, 1, v12
	v_mov_b32_e32 v13, v3
	v_lshl_add_u64 v[12:13], s[8:9], 0, v[12:13]
	s_lshl_b64 s[12:13], s[10:11], 1
	v_lshl_add_u64 v[12:13], v[12:13], 0, s[12:13]
	v_lshl_add_u64 v[12:13], v[12:13], 0, v[2:3]
	s_movk_i32 s7, 0x1000
	s_mov_b64 s[10:11], 0x1600
	v_add_co_u32_e32 v16, vcc, s7, v12
	v_lshl_add_u64 v[14:15], v[12:13], 0, s[10:11]
	s_nop 0
	v_addc_co_u32_e32 v17, vcc, 0, v13, vcc
	s_mov_b64 s[10:11], 0x3d600
	s_mov_b32 s7, 0x3d000
	global_load_dwordx2 v[152:153], v[14:15], off offset:16
	global_load_dwordx2 v[150:151], v[14:15], off offset:32
	global_load_dwordx2 v[148:149], v[14:15], off offset:48
	global_load_dwordx2 v[146:147], v[14:15], off offset:64
	global_load_dwordx2 v[154:155], v[16:17], off offset:1536
	global_load_dwordx2 v[144:145], v[14:15], off offset:80
	global_load_dwordx2 v[142:143], v[14:15], off offset:96
	global_load_dwordx2 v[140:141], v[14:15], off offset:112
	v_lshl_add_u64 v[14:15], v[12:13], 0, s[10:11]
	v_add_co_u32_e32 v12, vcc, s7, v12
	v_ashrrev_i32_e32 v62, 2, v178
	s_nop 0
	v_addc_co_u32_e32 v13, vcc, 0, v13, vcc
	global_load_dwordx2 v[136:137], v[14:15], off offset:16
	global_load_dwordx2 v[134:135], v[14:15], off offset:32
	global_load_dwordx2 v[132:133], v[14:15], off offset:48
	global_load_dwordx2 v[130:131], v[14:15], off offset:64
	global_load_dwordx2 v[138:139], v[12:13], off offset:1536
	global_load_dwordx2 v[128:129], v[14:15], off offset:80
	global_load_dwordx2 v[126:127], v[14:15], off offset:96
	global_load_dwordx2 v[124:125], v[14:15], off offset:112
	v_add_u32_e32 v14, s18, v62
	v_mov_b64_e32 v[12:13], s[8:9]
	v_mad_i64_i32 v[12:13], s[8:9], v14, s66, v[12:13]
	v_and_b32_e32 v164, 3, v178
	s_mov_b64 s[8:9], 0x1a00
	v_lshl_add_u64 v[16:17], v[12:13], 0, s[8:9]
	v_lshlrev_b32_e32 v160, 8, v164
	v_mov_b32_e32 v161, v3
	v_lshl_add_u64 v[18:19], v[16:17], 0, v[160:161]
	s_waitcnt lgkmcnt(0)
	s_barrier
	global_load_dwordx4 v[56:59], v[18:19], off
	global_load_dwordx4 v[64:67], v[18:19], off offset:16
	global_load_dwordx4 v[180:183], v[18:19], off offset:32
	global_load_dwordx4 v[184:187], v[18:19], off offset:48
	global_load_dwordx4 v[52:55], v[18:19], off offset:112
	global_load_dwordx4 v[188:191], v[18:19], off offset:96
	global_load_dwordx4 v[192:195], v[18:19], off offset:80
	global_load_dwordx4 v[196:199], v[18:19], off offset:64
	global_load_dwordx4 v[36:39], v[18:19], off offset:176
	global_load_dwordx4 v[40:43], v[18:19], off offset:160
	global_load_dwordx4 v[44:47], v[18:19], off offset:144
	global_load_dwordx4 v[48:51], v[18:19], off offset:128
	global_load_dwordx4 v[12:15], v[18:19], off offset:240
	global_load_dwordx4 v[20:23], v[18:19], off offset:224
	global_load_dwordx4 v[24:27], v[18:19], off offset:208
	global_load_dwordx4 v[32:35], v[18:19], off offset:192
	s_lshl_b32 s38, s6, 9
	v_lshlrev_b32_e32 v28, 7, v164
	v_mov_b32_e32 v29, v3
	v_lshl_add_u64 v[16:17], v[16:17], 0, s[38:39]
	v_lshl_add_u64 v[60:61], v[16:17], 0, v[28:29]
	global_load_dwordx4 v[16:19], v[60:61], off offset:16
	global_load_dwordx4 v[28:31], v[60:61], off
	s_load_dwordx4 s[8:11], s[56:57], 0xb0
	s_load_dwordx2 s[58:59], s[56:57], 0xc8
	s_lshl_b32 s6, s6, 10
	v_mul_u32_u24_e32 v164, 0x4400, v164
	s_waitcnt lgkmcnt(0)
	s_add_u32 s8, s8, s6
	s_addc_u32 s9, s9, 0
	s_add_u32 s10, s10, s6
	s_addc_u32 s11, s11, 0
	s_mov_b32 s6, 0x3b000000
	s_waitcnt vmcnt(17)
; __device__ __forceinline__ void cvt8(const u32x4 r, float (&f)[8]) { f[0] = bflo(r.x); f[1] = bfhi(r.x); f[2] = bflo(r.y); f[3] = bfhi(r.y); f[4] = bflo(r.z); f[5] = bfhi(r.z); f[6] = bflo(r.w); f[7] = bfhi(r.w); }
; __device__ __forceinline__ void gmlp_unit(Ctx& C, int l, int uidx) {
;     ...
;         float s = 0.f, q = 0.f;
; #pragma unroll
;         for (int c8 = 0; c8 < 16; ++c8) { float f[8]; cvt8(r1[c8], f);
; #pragma unroll
;             for (int j = 0; j < 8; ++j) { s += f[j]; q += f[j] * f[j]; } }
	v_lshlrev_b32_e32 v63, 16, v56
	v_and_b32_e32 v56, 0xffff0000, v56
	v_add_f32_e32 v200, 0, v63
	v_lshlrev_b32_e32 v157, 16, v57
	v_add_f32_e32 v200, v200, v56
	v_mul_f32_e32 v56, v56, v56
	v_and_b32_e32 v57, 0xffff0000, v57
	v_fmac_f32_e32 v56, v63, v63
	v_add_f32_e32 v63, v200, v157
	v_lshlrev_b32_e32 v161, 16, v58
	v_fmac_f32_e32 v56, v157, v157
	v_add_f32_e32 v63, v63, v57
	v_and_b32_e32 v58, 0xffff0000, v58
	v_fmac_f32_e32 v56, v57, v57
	v_add_f32_e32 v57, v63, v161
	v_lshlrev_b32_e32 v179, 16, v59
	v_fmac_f32_e32 v56, v161, v161
	v_add_f32_e32 v57, v57, v58
	v_and_b32_e32 v59, 0xffff0000, v59
	v_fmac_f32_e32 v56, v58, v58
	v_add_f32_e32 v57, v57, v179
	v_fmac_f32_e32 v56, v179, v179
	v_add_f32_e32 v57, v57, v59
	s_waitcnt vmcnt(16)
	v_lshlrev_b32_e32 v58, 16, v64
	v_fmac_f32_e32 v56, v59, v59
	v_and_b32_e32 v59, 0xffff0000, v64
	v_add_f32_e32 v57, v57, v58
	v_lshlrev_b32_e32 v63, 16, v65
	v_fmac_f32_e32 v56, v58, v58
	v_add_f32_e32 v57, v57, v59
	v_and_b32_e32 v64, 0xffff0000, v65
	v_fmac_f32_e32 v56, v59, v59
	v_add_f32_e32 v57, v57, v63
	v_lshlrev_b32_e32 v65, 16, v66
	v_fmac_f32_e32 v56, v63, v63
	v_add_f32_e32 v57, v57, v64
	v_and_b32_e32 v66, 0xffff0000, v66
	v_fmac_f32_e32 v56, v64, v64
	v_add_f32_e32 v57, v57, v65
	v_lshlrev_b32_e32 v157, 16, v67
	v_fmac_f32_e32 v56, v65, v65
	v_add_f32_e32 v57, v57, v66
	v_and_b32_e32 v67, 0xffff0000, v67
	v_fmac_f32_e32 v56, v66, v66
	v_add_f32_e32 v57, v57, v157
	v_fmac_f32_e32 v56, v157, v157
	v_add_f32_e32 v57, v57, v67
	s_waitcnt vmcnt(15)
	v_lshlrev_b32_e32 v58, 16, v180
	v_fmac_f32_e32 v56, v67, v67
	v_and_b32_e32 v59, 0xffff0000, v180
	v_add_f32_e32 v57, v57, v58
	v_lshlrev_b32_e32 v63, 16, v181
	v_fmac_f32_e32 v56, v58, v58
	v_add_f32_e32 v57, v57, v59
	v_and_b32_e32 v64, 0xffff0000, v181
	v_fmac_f32_e32 v56, v59, v59
	v_add_f32_e32 v57, v57, v63
	v_lshlrev_b32_e32 v65, 16, v182
	v_fmac_f32_e32 v56, v63, v63
	v_add_f32_e32 v57, v57, v64
	v_and_b32_e32 v66, 0xffff0000, v182
	v_fmac_f32_e32 v56, v64, v64
	v_add_f32_e32 v57, v57, v65
	v_lshlrev_b32_e32 v67, 16, v183
	v_fmac_f32_e32 v56, v65, v65
	v_add_f32_e32 v57, v57, v66
	v_and_b32_e32 v157, 0xffff0000, v183
	v_fmac_f32_e32 v56, v66, v66
	v_add_f32_e32 v57, v57, v67
	v_fmac_f32_e32 v56, v67, v67
	v_add_f32_e32 v57, v57, v157
	s_waitcnt vmcnt(14)
	v_lshlrev_b32_e32 v58, 16, v184
	v_fmac_f32_e32 v56, v157, v157
	v_and_b32_e32 v59, 0xffff0000, v184
	v_add_f32_e32 v57, v57, v58
	v_lshlrev_b32_e32 v63, 16, v185
	v_fmac_f32_e32 v56, v58, v58
	v_add_f32_e32 v57, v57, v59
	v_and_b32_e32 v64, 0xffff0000, v185
	v_fmac_f32_e32 v56, v59, v59
	v_add_f32_e32 v57, v57, v63
	v_lshlrev_b32_e32 v65, 16, v186
	v_fmac_f32_e32 v56, v63, v63
	v_add_f32_e32 v57, v57, v64
	v_and_b32_e32 v66, 0xffff0000, v186
	v_fmac_f32_e32 v56, v64, v64
	v_add_f32_e32 v57, v57, v65
	v_lshlrev_b32_e32 v67, 16, v187
	v_fmac_f32_e32 v56, v65, v65
	v_add_f32_e32 v57, v57, v66
	v_and_b32_e32 v157, 0xffff0000, v187
	v_fmac_f32_e32 v56, v66, v66
	v_add_f32_e32 v57, v57, v67
	v_fmac_f32_e32 v56, v67, v67
	v_add_f32_e32 v57, v57, v157
	s_waitcnt vmcnt(10)
	v_lshlrev_b32_e32 v58, 16, v196
	v_fmac_f32_e32 v56, v157, v157
	v_and_b32_e32 v59, 0xffff0000, v196
	v_add_f32_e32 v57, v57, v58
	v_lshlrev_b32_e32 v63, 16, v197
	v_fmac_f32_e32 v56, v58, v58
	v_add_f32_e32 v57, v57, v59
	v_and_b32_e32 v64, 0xffff0000, v197
	v_fmac_f32_e32 v56, v59, v59
	v_add_f32_e32 v57, v57, v63
	v_lshlrev_b32_e32 v65, 16, v198
	v_fmac_f32_e32 v56, v63, v63
	v_add_f32_e32 v57, v57, v64
	v_and_b32_e32 v66, 0xffff0000, v198
	v_fmac_f32_e32 v56, v64, v64
	v_add_f32_e32 v57, v57, v65
	v_lshlrev_b32_e32 v67, 16, v199
	v_fmac_f32_e32 v56, v65, v65
	v_add_f32_e32 v57, v57, v66
	v_and_b32_e32 v157, 0xffff0000, v199
	v_fmac_f32_e32 v56, v66, v66
	v_add_f32_e32 v57, v57, v67
	v_fmac_f32_e32 v56, v67, v67
	v_add_f32_e32 v57, v57, v157
	v_lshlrev_b32_e32 v58, 16, v192
	v_fmac_f32_e32 v56, v157, v157
	v_and_b32_e32 v59, 0xffff0000, v192
	v_add_f32_e32 v57, v57, v58
	v_lshlrev_b32_e32 v63, 16, v193
	v_fmac_f32_e32 v56, v58, v58
	v_add_f32_e32 v57, v57, v59
	v_and_b32_e32 v64, 0xffff0000, v193
	v_fmac_f32_e32 v56, v59, v59
	v_add_f32_e32 v57, v57, v63
	v_lshlrev_b32_e32 v65, 16, v194
	v_fmac_f32_e32 v56, v63, v63
	v_add_f32_e32 v57, v57, v64
	v_and_b32_e32 v66, 0xffff0000, v194
	v_fmac_f32_e32 v56, v64, v64
	v_add_f32_e32 v57, v57, v65
	v_lshlrev_b32_e32 v67, 16, v195
	v_fmac_f32_e32 v56, v65, v65
	v_add_f32_e32 v57, v57, v66
	v_and_b32_e32 v157, 0xffff0000, v195
	v_fmac_f32_e32 v56, v66, v66
	v_add_f32_e32 v57, v57, v67
	v_fmac_f32_e32 v56, v67, v67
	v_add_f32_e32 v57, v57, v157
	v_lshlrev_b32_e32 v58, 16, v188
	v_fmac_f32_e32 v56, v157, v157
	v_and_b32_e32 v59, 0xffff0000, v188
	v_add_f32_e32 v57, v57, v58
	v_lshlrev_b32_e32 v63, 16, v189
	v_fmac_f32_e32 v56, v58, v58
	v_add_f32_e32 v57, v57, v59
	v_and_b32_e32 v64, 0xffff0000, v189
	v_fmac_f32_e32 v56, v59, v59
	v_add_f32_e32 v57, v57, v63
	v_lshlrev_b32_e32 v65, 16, v190
	v_fmac_f32_e32 v56, v63, v63
	v_add_f32_e32 v57, v57, v64
	v_and_b32_e32 v66, 0xffff0000, v190
	v_fmac_f32_e32 v56, v64, v64
	v_add_f32_e32 v57, v57, v65
	v_lshlrev_b32_e32 v67, 16, v191
	v_fmac_f32_e32 v56, v65, v65
	v_add_f32_e32 v57, v57, v66
	v_and_b32_e32 v157, 0xffff0000, v191
	v_fmac_f32_e32 v56, v66, v66
	v_add_f32_e32 v57, v57, v67
	v_fmac_f32_e32 v56, v67, v67
	v_add_f32_e32 v57, v57, v157
	v_lshlrev_b32_e32 v58, 16, v52
	v_fmac_f32_e32 v56, v157, v157
	v_and_b32_e32 v52, 0xffff0000, v52
	v_add_f32_e32 v57, v57, v58
	v_lshlrev_b32_e32 v59, 16, v53
	v_fmac_f32_e32 v56, v58, v58
	v_add_f32_e32 v57, v57, v52
	v_and_b32_e32 v53, 0xffff0000, v53
	v_fmac_f32_e32 v56, v52, v52
	v_add_f32_e32 v52, v57, v59
	v_lshlrev_b32_e32 v63, 16, v54
	v_fmac_f32_e32 v56, v59, v59
	v_add_f32_e32 v52, v52, v53
	v_and_b32_e32 v54, 0xffff0000, v54
	v_fmac_f32_e32 v56, v53, v53
	v_add_f32_e32 v52, v52, v63
	v_lshlrev_b32_e32 v64, 16, v55
	v_fmac_f32_e32 v56, v63, v63
	v_add_f32_e32 v52, v52, v54
	v_and_b32_e32 v55, 0xffff0000, v55
	v_fmac_f32_e32 v56, v54, v54
	v_add_f32_e32 v52, v52, v64
	v_fmac_f32_e32 v56, v64, v64
	v_add_f32_e32 v52, v52, v55
	s_waitcnt vmcnt(6)
; template <int CTRL> __device__ __forceinline__ float dpp_f(float x) { return __int_as_float(__builtin_amdgcn_update_dpp(0, __float_as_int(x), CTRL, 0xF, 0xF, true)); }
; __device__ __forceinline__ void cvt8(const u32x4 r, float (&f)[8]) { f[0] = bflo(r.x); f[1] = bfhi(r.x); f[2] = bflo(r.y); f[3] = bfhi(r.y); f[4] = bflo(r.z); f[5] = bfhi(r.z); f[6] = bflo(r.w); f[7] = bfhi(r.w); }
; __device__ __forceinline__ void gmlp_unit(Ctx& C, int l, int uidx) {
;     ...
;         float s = 0.f, q = 0.f;
; #pragma unroll
;         for (int c8 = 0; c8 < 16; ++c8) { float f[8]; cvt8(r1[c8], f);
; #pragma unroll
;             for (int j = 0; j < 8; ++j) { s += f[j]; q += f[j] * f[j]; } }
;         s += dpp_f<DPP_XOR1>(s); s += dpp_f<DPP_XOR2>(s); q += dpp_f<DPP_XOR1>(q); q += dpp_f<DPP_XOR2>(q);
;         const float mean = s * (1.0f / 512.0f); const float var = fmaxf(q * (1.0f / 512.0f) - mean * mean, 0.f); const float rstd = 1.0f / sqrtf(var + LN_EPS);
;         const float* lg = INP(I_GLG) + l * 512 + 256 * hf + 64 * part; const float* lb = INP(I_GLB) + l * 512 + 256 * hf + 64 * part;
; #pragma unroll
;         for (int c8 = 0; c8 < 8; ++c8) { float f[8]; cvt8(r2[c8], f);
;             const f32x4 g0 = *(const f32x4*)(lg + 8 * c8), g1 = *(const f32x4*)(lg + 8 * c8 + 4), b0 = *(const f32x4*)(lb + 8 * c8), b1 = *(const f32x4*)(lb + 8 * c8 + 4);
	v_lshlrev_b32_e32 v53, 16, v48
	v_fmac_f32_e32 v56, v55, v55
	v_and_b32_e32 v48, 0xffff0000, v48
	v_add_f32_e32 v52, v52, v53
	v_lshlrev_b32_e32 v54, 16, v49
	v_fmac_f32_e32 v56, v53, v53
	v_add_f32_e32 v52, v52, v48
	v_and_b32_e32 v49, 0xffff0000, v49
	v_fmac_f32_e32 v56, v48, v48
	v_add_f32_e32 v48, v52, v54
	v_lshlrev_b32_e32 v55, 16, v50
	v_fmac_f32_e32 v56, v54, v54
	v_add_f32_e32 v48, v48, v49
	v_and_b32_e32 v50, 0xffff0000, v50
	v_fmac_f32_e32 v56, v49, v49
	v_add_f32_e32 v48, v48, v55
	v_lshlrev_b32_e32 v57, 16, v51
	v_fmac_f32_e32 v56, v55, v55
	v_add_f32_e32 v48, v48, v50
	v_and_b32_e32 v51, 0xffff0000, v51
	v_fmac_f32_e32 v56, v50, v50
	v_add_f32_e32 v48, v48, v57
	v_fmac_f32_e32 v56, v57, v57
	v_add_f32_e32 v48, v48, v51
	v_lshlrev_b32_e32 v49, 16, v44
	v_fmac_f32_e32 v56, v51, v51
	v_and_b32_e32 v44, 0xffff0000, v44
	v_add_f32_e32 v48, v48, v49
	v_lshlrev_b32_e32 v50, 16, v45
	v_fmac_f32_e32 v56, v49, v49
	v_add_f32_e32 v48, v48, v44
	v_and_b32_e32 v45, 0xffff0000, v45
	v_fmac_f32_e32 v56, v44, v44
	v_add_f32_e32 v44, v48, v50
	v_lshlrev_b32_e32 v51, 16, v46
	v_fmac_f32_e32 v56, v50, v50
	v_add_f32_e32 v44, v44, v45
	v_and_b32_e32 v46, 0xffff0000, v46
	v_fmac_f32_e32 v56, v45, v45
	v_add_f32_e32 v44, v44, v51
	v_lshlrev_b32_e32 v52, 16, v47
	v_fmac_f32_e32 v56, v51, v51
	v_add_f32_e32 v44, v44, v46
	v_and_b32_e32 v47, 0xffff0000, v47
	v_fmac_f32_e32 v56, v46, v46
	v_add_f32_e32 v44, v44, v52
	v_fmac_f32_e32 v56, v52, v52
	v_add_f32_e32 v44, v44, v47
	v_lshlrev_b32_e32 v45, 16, v40
	v_fmac_f32_e32 v56, v47, v47
	v_and_b32_e32 v40, 0xffff0000, v40
	v_add_f32_e32 v44, v44, v45
	v_lshlrev_b32_e32 v46, 16, v41
	v_fmac_f32_e32 v56, v45, v45
	v_add_f32_e32 v44, v44, v40
	v_and_b32_e32 v41, 0xffff0000, v41
	v_fmac_f32_e32 v56, v40, v40
	v_add_f32_e32 v40, v44, v46
	v_lshlrev_b32_e32 v47, 16, v42
	v_fmac_f32_e32 v56, v46, v46
	v_add_f32_e32 v40, v40, v41
	v_and_b32_e32 v42, 0xffff0000, v42
	v_fmac_f32_e32 v56, v41, v41
	v_add_f32_e32 v40, v40, v47
	v_lshlrev_b32_e32 v48, 16, v43
	v_fmac_f32_e32 v56, v47, v47
	v_add_f32_e32 v40, v40, v42
	v_and_b32_e32 v43, 0xffff0000, v43
	v_fmac_f32_e32 v56, v42, v42
	v_add_f32_e32 v40, v40, v48
	v_fmac_f32_e32 v56, v48, v48
	v_add_f32_e32 v40, v40, v43
	v_lshlrev_b32_e32 v41, 16, v36
	v_fmac_f32_e32 v56, v43, v43
	v_and_b32_e32 v36, 0xffff0000, v36
	v_add_f32_e32 v40, v40, v41
	v_lshlrev_b32_e32 v42, 16, v37
	v_fmac_f32_e32 v56, v41, v41
	v_add_f32_e32 v40, v40, v36
	v_and_b32_e32 v37, 0xffff0000, v37
	v_fmac_f32_e32 v56, v36, v36
	v_add_f32_e32 v36, v40, v42
	v_lshlrev_b32_e32 v43, 16, v38
	v_fmac_f32_e32 v56, v42, v42
	v_add_f32_e32 v36, v36, v37
	v_and_b32_e32 v38, 0xffff0000, v38
	v_fmac_f32_e32 v56, v37, v37
	v_add_f32_e32 v36, v36, v43
	v_lshlrev_b32_e32 v44, 16, v39
	v_fmac_f32_e32 v56, v43, v43
	v_add_f32_e32 v36, v36, v38
	v_and_b32_e32 v39, 0xffff0000, v39
	v_fmac_f32_e32 v56, v38, v38
	v_add_f32_e32 v36, v36, v44
	v_fmac_f32_e32 v56, v44, v44
	v_add_f32_e32 v36, v36, v39
	s_waitcnt vmcnt(2)
	v_lshlrev_b32_e32 v37, 16, v32
	v_fmac_f32_e32 v56, v39, v39
	v_and_b32_e32 v32, 0xffff0000, v32
	v_add_f32_e32 v36, v36, v37
	v_lshlrev_b32_e32 v38, 16, v33
	v_fmac_f32_e32 v56, v37, v37
	v_add_f32_e32 v36, v36, v32
	v_and_b32_e32 v33, 0xffff0000, v33
	v_fmac_f32_e32 v56, v32, v32
	v_add_f32_e32 v32, v36, v38
	v_lshlrev_b32_e32 v39, 16, v34
	v_fmac_f32_e32 v56, v38, v38
	v_add_f32_e32 v32, v32, v33
	v_and_b32_e32 v34, 0xffff0000, v34
	v_fmac_f32_e32 v56, v33, v33
	v_add_f32_e32 v32, v32, v39
	v_lshlrev_b32_e32 v40, 16, v35
	v_fmac_f32_e32 v56, v39, v39
	v_add_f32_e32 v32, v32, v34
	v_and_b32_e32 v35, 0xffff0000, v35
	v_fmac_f32_e32 v56, v34, v34
	v_add_f32_e32 v32, v32, v40
	v_fmac_f32_e32 v56, v40, v40
	v_add_f32_e32 v32, v32, v35
	v_lshlrev_b32_e32 v33, 16, v24
	v_fmac_f32_e32 v56, v35, v35
	v_and_b32_e32 v24, 0xffff0000, v24
	v_add_f32_e32 v32, v32, v33
	v_lshlrev_b32_e32 v34, 16, v25
	v_fmac_f32_e32 v56, v33, v33
	v_add_f32_e32 v32, v32, v24
	v_and_b32_e32 v25, 0xffff0000, v25
	v_fmac_f32_e32 v56, v24, v24
	v_add_f32_e32 v24, v32, v34
	v_lshlrev_b32_e32 v35, 16, v26
	v_fmac_f32_e32 v56, v34, v34
	v_add_f32_e32 v24, v24, v25
	v_and_b32_e32 v26, 0xffff0000, v26
	v_fmac_f32_e32 v56, v25, v25
	v_add_f32_e32 v24, v24, v35
	v_lshlrev_b32_e32 v36, 16, v27
	v_fmac_f32_e32 v56, v35, v35
	v_add_f32_e32 v24, v24, v26
	v_and_b32_e32 v27, 0xffff0000, v27
	v_fmac_f32_e32 v56, v26, v26
	v_add_f32_e32 v24, v24, v36
	v_fmac_f32_e32 v56, v36, v36
	v_add_f32_e32 v24, v24, v27
	v_lshlrev_b32_e32 v25, 16, v20
	v_fmac_f32_e32 v56, v27, v27
	v_and_b32_e32 v20, 0xffff0000, v20
	v_add_f32_e32 v24, v24, v25
	v_lshlrev_b32_e32 v26, 16, v21
	v_fmac_f32_e32 v56, v25, v25
	v_add_f32_e32 v24, v24, v20
	v_and_b32_e32 v21, 0xffff0000, v21
	v_fmac_f32_e32 v56, v20, v20
	v_add_f32_e32 v20, v24, v26
	v_lshlrev_b32_e32 v27, 16, v22
	v_fmac_f32_e32 v56, v26, v26
	v_add_f32_e32 v20, v20, v21
	v_and_b32_e32 v22, 0xffff0000, v22
	v_fmac_f32_e32 v56, v21, v21
	v_add_f32_e32 v20, v20, v27
	v_lshlrev_b32_e32 v32, 16, v23
	v_fmac_f32_e32 v56, v27, v27
	v_add_f32_e32 v20, v20, v22
	v_and_b32_e32 v23, 0xffff0000, v23
	v_fmac_f32_e32 v56, v22, v22
	v_add_f32_e32 v20, v20, v32
	v_fmac_f32_e32 v56, v32, v32
	v_add_f32_e32 v20, v20, v23
	v_lshlrev_b32_e32 v21, 16, v12
	v_fmac_f32_e32 v56, v23, v23
	v_and_b32_e32 v12, 0xffff0000, v12
	v_add_f32_e32 v20, v20, v21
	v_lshlrev_b32_e32 v22, 16, v13
	v_fmac_f32_e32 v56, v21, v21
	v_add_f32_e32 v20, v20, v12
	v_and_b32_e32 v13, 0xffff0000, v13
	v_fmac_f32_e32 v56, v12, v12
	v_add_f32_e32 v12, v20, v22
	v_lshlrev_b32_e32 v23, 16, v14
	v_add_f32_e32 v12, v12, v13
	v_and_b32_e32 v14, 0xffff0000, v14
	v_fmac_f32_e32 v56, v22, v22
	v_add_f32_e32 v12, v12, v23
	v_lshlrev_b32_e32 v24, 16, v15
	v_fmac_f32_e32 v56, v13, v13
	v_add_f32_e32 v12, v12, v14
	v_and_b32_e32 v15, 0xffff0000, v15
	v_fmac_f32_e32 v56, v23, v23
	v_add_f32_e32 v12, v12, v24
	v_fmac_f32_e32 v56, v14, v14
	v_add_f32_e32 v12, v12, v15
	global_load_dwordx4 v[180:183], v160, s[8:9]
	global_load_dwordx4 v[184:187], v160, s[10:11]
	v_fmac_f32_e32 v56, v24, v24
	v_add_f32_dpp v12, v12, v12 quad_perm:[1,0,3,2] row_mask:0xf bank_mask:0xf bound_ctrl:1
	v_fmac_f32_e32 v56, v15, v15
	global_load_dwordx4 v[44:47], v160, s[8:9] offset:16
	global_load_dwordx4 v[48:51], v160, s[10:11] offset:16
	v_add_f32_dpp v157, v12, v12 quad_perm:[2,3,0,1] row_mask:0xf bank_mask:0xf bound_ctrl:1
	v_add_f32_dpp v12, v56, v56 quad_perm:[1,0,3,2] row_mask:0xf bank_mask:0xf bound_ctrl:1
	v_mul_f32_e32 v13, 0x3b000000, v157
	v_mul_f32_e32 v13, v13, v13
	v_add_f32_dpp v12, v12, v12 quad_perm:[2,3,0,1] row_mask:0xf bank_mask:0xf bound_ctrl:1
	v_fma_f32 v12, v12, s6, -v13
	v_max_f32_e32 v12, 0, v12
	v_add_f32_e32 v12, 0x358637bd, v12
	s_mov_b32 s6, 0xf800000
	v_mul_f32_e32 v13, 0x4f800000, v12
	v_cmp_gt_f32_e32 vcc, s6, v12
	v_lshlrev_b32_e32 v179, 1, v62
	s_waitcnt vmcnt(4)
; #define LAS __attribute__((address_space(3)))
; __device__ __forceinline__ unsigned pk2(float lo, float hi) { f32x2 v = {lo, hi}; bf16x2_t b = __builtin_convertvector(v, bf16x2_t); return __builtin_bit_cast(unsigned, b); }
; __device__ __forceinline__ void cvt8(const u32x4 r, float (&f)[8]) { f[0] = bflo(r.x); f[1] = bfhi(r.x); f[2] = bflo(r.y); f[3] = bfhi(r.y); f[4] = bflo(r.z); f[5] = bfhi(r.z); f[6] = bflo(r.w); f[7] = bfhi(r.w); }
; __device__ __forceinline__ void gmlp_unit(Ctx& C, int l, int uidx) {
;     ...
;         const float mean = s * (1.0f / 512.0f); const float var = fmaxf(q * (1.0f / 512.0f) - mean * mean, 0.f); const float rstd = 1.0f / sqrtf(var + LN_EPS);
;         const float* lg = INP(I_GLG) + l * 512 + 256 * hf + 64 * part; const float* lb = INP(I_GLB) + l * 512 + 256 * hf + 64 * part;
; #pragma unroll
;         for (int c8 = 0; c8 < 8; ++c8) { float f[8]; cvt8(r2[c8], f);
;             const f32x4 g0 = *(const f32x4*)(lg + 8 * c8), g1 = *(const f32x4*)(lg + 8 * c8 + 4), b0 = *(const f32x4*)(lb + 8 * c8), b1 = *(const f32x4*)(lb + 8 * c8 + 4);
;             const float gg[8] = {g0[0], g0[1], g0[2], g0[3], g1[0], g1[1], g1[2], g1[3]}, bb[8] = {b0[0], b0[1], b0[2], b0[3], b1[0], b1[1], b1[2], b1[3]};
; #pragma unroll
;             for (int j = 0; j < 8; ++j) { const float vn = (f[j] - mean) * rstd * gg[j] + bb[j];
;                 *(LAS bf16*)(C.lds + (64 * part + 8 * c8 + j) * VS + tok * 2) = (bf16)(pk2(vn, 0.f) & 0xffffu); } }
	v_lshlrev_b32_e32 v188, 16, v28
	v_cndmask_b32_e32 v24, v12, v13, vcc
	v_sqrt_f32_e32 v25, v24
	global_load_dwordx4 v[36:39], v[60:61], off offset:48
	global_load_dwordx4 v[40:43], v[60:61], off offset:32
	global_load_dwordx4 v[12:15], v[60:61], off offset:112
	global_load_dwordx4 v[20:23], v[60:61], off offset:96
	v_and_b32_e32 v28, 0xffff0000, v28
	v_fmac_f32_e32 v28, 0xbb000000, v157
	v_add_u32_e32 v26, -1, v25
	v_fma_f32 v27, -v26, v25, v24
	v_cmp_ge_f32_e64 s[6:7], 0, v27
	v_add_u32_e32 v27, 1, v25
	v_lshlrev_b32_e32 v189, 16, v29
	v_cndmask_b32_e64 v26, v25, v26, s[6:7]
	v_fma_f32 v25, -v27, v25, v24
	v_cmp_lt_f32_e64 s[6:7], 0, v25
	v_add3_u32 v164, 0, v179, v164
	v_fmac_f32_e32 v189, 0xbb000000, v157
	v_cndmask_b32_e64 v25, v26, v27, s[6:7]
	v_mul_f32_e32 v26, 0x37800000, v25
	v_cndmask_b32_e32 v25, v25, v26, vcc
	v_cmp_class_f32_e32 vcc, v24, v163
	v_and_b32_e32 v29, 0xffff0000, v29
	v_fmac_f32_e32 v29, 0xbb000000, v157
	v_cndmask_b32_e32 v63, v25, v24, vcc
	v_div_scale_f32 v64, s[6:7], v63, v63, 1.0
	v_rcp_f32_e32 v65, v64
	global_load_dwordx4 v[52:55], v160, s[8:9] offset:32
	global_load_dwordx4 v[56:59], v160, s[10:11] offset:32
	global_load_dwordx4 v[24:27], v[60:61], off offset:80
	global_load_dwordx4 v[32:35], v[60:61], off offset:64
	v_lshlrev_b32_e32 v190, 16, v30
	v_fmac_f32_e32 v188, 0xbb000000, v157
	v_fma_f32 v60, -v64, v65, 1.0
	v_fmac_f32_e32 v65, v60, v65
	v_div_scale_f32 v60, vcc, 1.0, v63, 1.0
	v_mul_f32_e32 v61, v60, v65
	v_fma_f32 v66, -v64, v61, v60
	v_fmac_f32_e32 v61, v66, v65
	v_fma_f32 v60, -v64, v61, v60
	v_div_fmas_f32 v60, v60, v65, v61
	v_div_fixup_f32 v161, v60, v63, 1.0
	global_load_dwordx4 v[60:63], v160, s[8:9] offset:48
	global_load_dwordx4 v[64:67], v160, s[10:11] offset:48
	v_mul_f32_e32 v28, v28, v161
	v_fmac_f32_e32 v190, 0xbb000000, v157
	v_mul_f32_e32 v188, v188, v161
	v_and_b32_e32 v30, 0xffff0000, v30
	v_fmac_f32_e32 v30, 0xbb000000, v157
	v_lshlrev_b32_e32 v191, 16, v31
	v_fmac_f32_e32 v191, 0xbb000000, v157
	v_and_b32_e32 v31, 0xffff0000, v31
	v_fmac_f32_e32 v31, 0xbb000000, v157
	s_movk_i32 s6, 0x110
	s_waitcnt vmcnt(12)
	v_fma_f32 v28, v181, v28, v185
	v_cvt_pk_bf16_f32 v28, v28, s0
	ds_write_b16 v164, v28 offset:272
	v_mul_f32_e32 v28, v189, v161
	v_fma_f32 v28, v182, v28, v186
	v_cvt_pk_bf16_f32 v28, v28, s0
	ds_write_b16 v164, v28 offset:544
	v_mul_f32_e32 v28, v29, v161
	v_fmac_f32_e32 v187, v183, v28
	v_cvt_pk_bf16_f32 v28, v187, s0
	ds_write_b16 v164, v28 offset:816
	v_mul_f32_e32 v28, v190, v161
	v_fma_f32 v180, v180, v188, v184
	s_waitcnt vmcnt(10)
	v_fma_f32 v28, v44, v28, v48
	v_cvt_pk_bf16_f32 v180, v180, s0
	v_cvt_pk_bf16_f32 v28, v28, s0
	ds_write_b16 v164, v180
	ds_write_b16 v164, v28 offset:1088
	v_mul_f32_e32 v28, v30, v161
	global_load_dwordx4 v[180:183], v160, s[8:9] offset:64
	global_load_dwordx4 v[184:187], v160, s[10:11] offset:64
	v_fma_f32 v28, v45, v28, v49
	v_cvt_pk_bf16_f32 v28, v28, s0
	ds_write_b16 v164, v28 offset:1360
	v_mul_f32_e32 v28, v191, v161
	v_fma_f32 v28, v46, v28, v50
	v_cvt_pk_bf16_f32 v28, v28, s0
	ds_write_b16 v164, v28 offset:1632
	v_mul_f32_e32 v28, v31, v161
	v_fmac_f32_e32 v51, v47, v28
	v_cvt_pk_bf16_f32 v28, v51, s0
	ds_write_b16 v164, v28 offset:1904
	global_load_dwordx4 v[28:31], v160, s[8:9] offset:80
	global_load_dwordx4 v[48:51], v160, s[10:11] offset:80
	v_lshlrev_b32_e32 v44, 16, v16
	v_and_b32_e32 v16, 0xffff0000, v16
	v_fmac_f32_e32 v16, 0xbb000000, v157
	v_mul_f32_e32 v16, v16, v161
	v_lshlrev_b32_e32 v45, 16, v17
	v_fmac_f32_e32 v45, 0xbb000000, v157
	v_and_b32_e32 v17, 0xffff0000, v17
	v_fmac_f32_e32 v17, 0xbb000000, v157
	v_lshlrev_b32_e32 v46, 16, v18
	s_waitcnt vmcnt(8)
	v_fma_f32 v16, v53, v16, v57
	v_cvt_pk_bf16_f32 v16, v16, s0
	ds_write_b16 v164, v16 offset:2448
	v_mul_f32_e32 v16, v45, v161
	v_fma_f32 v16, v54, v16, v58
	v_cvt_pk_bf16_f32 v16, v16, s0
	ds_write_b16 v164, v16 offset:2720
	v_mul_f32_e32 v16, v17, v161
	v_fmac_f32_e32 v59, v55, v16
	v_fmac_f32_e32 v44, 0xbb000000, v157
	v_cvt_pk_bf16_f32 v16, v59, s0
	v_fmac_f32_e32 v46, 0xbb000000, v157
	v_mul_f32_e32 v44, v44, v161
	ds_write_b16 v164, v16 offset:2992
	v_mul_f32_e32 v16, v46, v161
	v_and_b32_e32 v18, 0xffff0000, v18
	v_fma_f32 v44, v52, v44, v56
	s_waitcnt vmcnt(4)
	v_fma_f32 v16, v60, v16, v64
	v_cvt_pk_bf16_f32 v44, v44, s0
	v_cvt_pk_bf16_f32 v16, v16, s0
	v_fmac_f32_e32 v18, 0xbb000000, v157
	ds_write_b16 v164, v44 offset:2176
	ds_write_b16 v164, v16 offset:3264
	v_mul_f32_e32 v16, v18, v161
	v_lshlrev_b32_e32 v47, 16, v19
	global_load_dwordx4 v[52:55], v160, s[8:9] offset:96
	global_load_dwordx4 v[56:59], v160, s[10:11] offset:96
	v_fma_f32 v16, v61, v16, v65
	v_cvt_pk_bf16_f32 v16, v16, s0
	v_fmac_f32_e32 v47, 0xbb000000, v157
	ds_write_b16 v164, v16 offset:3536
	v_mul_f32_e32 v16, v47, v161
	v_and_b32_e32 v19, 0xffff0000, v19
	v_fma_f32 v16, v62, v16, v66
	v_cvt_pk_bf16_f32 v16, v16, s0
	v_fmac_f32_e32 v19, 0xbb000000, v157
	ds_write_b16 v164, v16 offset:3808
	v_mul_f32_e32 v16, v19, v161
	v_fmac_f32_e32 v67, v63, v16
	v_cvt_pk_bf16_f32 v16, v67, s0
	ds_write_b16 v164, v16 offset:4080
	global_load_dwordx4 v[16:19], v160, s[8:9] offset:112
	global_load_dwordx4 v[44:47], v160, s[10:11] offset:112
	v_lshlrev_b32_e32 v60, 16, v40
	v_and_b32_e32 v40, 0xffff0000, v40
	v_fmac_f32_e32 v40, 0xbb000000, v157
	v_mul_f32_e32 v40, v40, v161
	v_lshlrev_b32_e32 v61, 16, v41
	v_fmac_f32_e32 v61, 0xbb000000, v157
	v_and_b32_e32 v41, 0xffff0000, v41
	v_fmac_f32_e32 v41, 0xbb000000, v157
	v_lshlrev_b32_e32 v62, 16, v42
	v_fmac_f32_e32 v60, 0xbb000000, v157
	v_fmac_f32_e32 v62, 0xbb000000, v157
	v_mul_f32_e32 v60, v60, v161
	v_and_b32_e32 v42, 0xffff0000, v42
	v_fmac_f32_e32 v42, 0xbb000000, v157
	v_lshlrev_b32_e32 v179, 16, v43
	v_fmac_f32_e32 v179, 0xbb000000, v157
	v_and_b32_e32 v43, 0xffff0000, v43
	s_waitcnt vmcnt(6)
; #define LAS __attribute__((address_space(3)))
; __device__ __forceinline__ unsigned pk2(float lo, float hi) { f32x2 v = {lo, hi}; bf16x2_t b = __builtin_convertvector(v, bf16x2_t); return __builtin_bit_cast(unsigned, b); }
; __device__ __forceinline__ void cvt8(const u32x4 r, float (&f)[8]) { f[0] = bflo(r.x); f[1] = bfhi(r.x); f[2] = bflo(r.y); f[3] = bfhi(r.y); f[4] = bflo(r.z); f[5] = bfhi(r.z); f[6] = bflo(r.w); f[7] = bfhi(r.w); }
; __device__ __forceinline__ void gmlp_unit(Ctx& C, int l, int uidx) {
;     ...
;         for (int c8 = 0; c8 < 8; ++c8) { float f[8]; cvt8(r2[c8], f);
;             const f32x4 g0 = *(const f32x4*)(lg + 8 * c8), g1 = *(const f32x4*)(lg + 8 * c8 + 4), b0 = *(const f32x4*)(lb + 8 * c8), b1 = *(const f32x4*)(lb + 8 * c8 + 4);
;             const float gg[8] = {g0[0], g0[1], g0[2], g0[3], g1[0], g1[1], g1[2], g1[3]}, bb[8] = {b0[0], b0[1], b0[2], b0[3], b1[0], b1[1], b1[2], b1[3]};
; #pragma unroll
;             for (int j = 0; j < 8; ++j) { const float vn = (f[j] - mean) * rstd * gg[j] + bb[j];
;                 *(LAS bf16*)(C.lds + (64 * part + 8 * c8 + j) * VS + tok * 2) = (bf16)(pk2(vn, 0.f) & 0xffffu); } }
	v_fma_f32 v40, v181, v40, v185
	v_cvt_pk_bf16_f32 v40, v40, s0
	ds_write_b16 v164, v40 offset:4624
	v_mul_f32_e32 v40, v61, v161
	v_fma_f32 v40, v182, v40, v186
	v_cvt_pk_bf16_f32 v40, v40, s0
	ds_write_b16 v164, v40 offset:4896
	v_mul_f32_e32 v40, v41, v161
	v_fmac_f32_e32 v187, v183, v40
	v_cvt_pk_bf16_f32 v40, v187, s0
	ds_write_b16 v164, v40 offset:5168
	v_mul_f32_e32 v40, v62, v161
	v_fma_f32 v60, v180, v60, v184
	s_waitcnt vmcnt(4)
	v_fma_f32 v28, v28, v40, v48
	v_cvt_pk_bf16_f32 v60, v60, s0
	v_cvt_pk_bf16_f32 v28, v28, s0
	ds_write_b16 v164, v60 offset:4352
	ds_write_b16 v164, v28 offset:5440
	v_mul_f32_e32 v28, v42, v161
	global_load_dwordx4 v[60:63], v160, s[8:9] offset:128
	global_load_dwordx4 v[64:67], v160, s[10:11] offset:128
	v_fma_f32 v28, v29, v28, v49
	v_cvt_pk_bf16_f32 v28, v28, s0
	ds_write_b16 v164, v28 offset:5712
	v_mul_f32_e32 v28, v179, v161
	v_fma_f32 v28, v30, v28, v50
	v_cvt_pk_bf16_f32 v28, v28, s0
	v_fmac_f32_e32 v43, 0xbb000000, v157
	ds_write_b16 v164, v28 offset:5984
	v_mul_f32_e32 v28, v43, v161
	v_fmac_f32_e32 v51, v31, v28
	v_cvt_pk_bf16_f32 v28, v51, s0
	ds_write_b16 v164, v28 offset:6256
	global_load_dwordx4 v[28:31], v160, s[8:9] offset:144
	global_load_dwordx4 v[40:43], v160, s[10:11] offset:144
	v_lshlrev_b32_e32 v48, 16, v36
	v_and_b32_e32 v36, 0xffff0000, v36
	v_fmac_f32_e32 v36, 0xbb000000, v157
	v_mul_f32_e32 v36, v36, v161
	v_lshlrev_b32_e32 v49, 16, v37
	v_fmac_f32_e32 v49, 0xbb000000, v157
	v_and_b32_e32 v37, 0xffff0000, v37
	v_fmac_f32_e32 v37, 0xbb000000, v157
	v_lshlrev_b32_e32 v50, 16, v38
	v_fmac_f32_e32 v50, 0xbb000000, v157
	v_fmac_f32_e32 v48, 0xbb000000, v157
	v_and_b32_e32 v179, 0xffff0000, v38
	v_mul_f32_e32 v38, v48, v161
	v_fmac_f32_e32 v179, 0xbb000000, v157
	s_waitcnt vmcnt(6)
	v_fma_f32 v36, v53, v36, v57
	v_cvt_pk_bf16_f32 v36, v36, s0
	ds_write_b16 v164, v36 offset:6800
	v_mul_f32_e32 v36, v49, v161
	v_fma_f32 v36, v54, v36, v58
	v_cvt_pk_bf16_f32 v36, v36, s0
	ds_write_b16 v164, v36 offset:7072
	v_mul_f32_e32 v36, v37, v161
	v_fmac_f32_e32 v59, v55, v36
	v_cvt_pk_bf16_f32 v36, v59, s0
	ds_write_b16 v164, v36 offset:7344
	v_mul_f32_e32 v36, v50, v161
	v_fma_f32 v38, v52, v38, v56
	v_cvt_pk_bf16_f32 v38, v38, s0
	v_lshlrev_b32_e32 v180, 16, v39
	s_waitcnt vmcnt(4)
	v_fma_f32 v16, v16, v36, v44
	v_cvt_pk_bf16_f32 v16, v16, s0
	ds_write_b16 v164, v16 offset:7616
	v_mul_f32_e32 v16, v179, v161
	ds_write_b16 v164, v38 offset:6528
	v_fma_f32 v16, v17, v16, v45
	v_and_b32_e32 v181, 0xffff0000, v39
	global_load_dwordx4 v[36:39], v160, s[8:9] offset:160
	global_load_dwordx4 v[48:51], v160, s[10:11] offset:160
	v_cvt_pk_bf16_f32 v16, v16, s0
	v_fmac_f32_e32 v180, 0xbb000000, v157
	ds_write_b16 v164, v16 offset:7888
	v_mul_f32_e32 v16, v180, v161
	v_fma_f32 v16, v18, v16, v46
	v_cvt_pk_bf16_f32 v16, v16, s0
	v_fmac_f32_e32 v181, 0xbb000000, v157
	ds_write_b16 v164, v16 offset:8160
	v_mul_f32_e32 v16, v181, v161
	v_fmac_f32_e32 v47, v19, v16
	v_cvt_pk_bf16_f32 v16, v47, s0
	ds_write_b16 v164, v16 offset:8432
	global_load_dwordx4 v[16:19], v160, s[8:9] offset:176
	global_load_dwordx4 v[44:47], v160, s[10:11] offset:176
	v_lshlrev_b32_e32 v52, 16, v32
	v_and_b32_e32 v32, 0xffff0000, v32
	v_fmac_f32_e32 v32, 0xbb000000, v157
	v_mul_f32_e32 v32, v32, v161
	v_lshlrev_b32_e32 v53, 16, v33
	v_fmac_f32_e32 v53, 0xbb000000, v157
	v_and_b32_e32 v33, 0xffff0000, v33
	v_fmac_f32_e32 v33, 0xbb000000, v157
	v_lshlrev_b32_e32 v54, 16, v34
	v_fmac_f32_e32 v52, 0xbb000000, v157
	v_fmac_f32_e32 v54, 0xbb000000, v157
	v_and_b32_e32 v56, 0xffff0000, v34
	v_mul_f32_e32 v34, v52, v161
	v_fmac_f32_e32 v56, 0xbb000000, v157
	v_lshlrev_b32_e32 v57, 16, v35
	v_and_b32_e32 v58, 0xffff0000, v35
	s_waitcnt vmcnt(6)
	v_fma_f32 v32, v61, v32, v65
	v_cvt_pk_bf16_f32 v32, v32, s0
	ds_write_b16 v164, v32 offset:8976
	v_mul_f32_e32 v32, v53, v161
	v_fma_f32 v32, v62, v32, v66
	v_cvt_pk_bf16_f32 v32, v32, s0
	ds_write_b16 v164, v32 offset:9248
	v_mul_f32_e32 v32, v33, v161
	v_fmac_f32_e32 v67, v63, v32
	v_cvt_pk_bf16_f32 v32, v67, s0
	ds_write_b16 v164, v32 offset:9520
	v_mul_f32_e32 v32, v54, v161
	v_fma_f32 v34, v60, v34, v64
	s_waitcnt vmcnt(4)
	v_fma_f32 v28, v28, v32, v40
	v_cvt_pk_bf16_f32 v34, v34, s0
	v_cvt_pk_bf16_f32 v28, v28, s0
	ds_write_b16 v164, v34 offset:8704
	ds_write_b16 v164, v28 offset:9792
	v_mul_f32_e32 v28, v56, v161
	global_load_dwordx4 v[32:35], v160, s[8:9] offset:192
	global_load_dwordx4 v[52:55], v160, s[10:11] offset:192
	v_fma_f32 v28, v29, v28, v41
	v_cvt_pk_bf16_f32 v28, v28, s0
	v_fmac_f32_e32 v57, 0xbb000000, v157
	ds_write_b16 v164, v28 offset:10064
	v_mul_f32_e32 v28, v57, v161
	v_fma_f32 v28, v30, v28, v42
	v_cvt_pk_bf16_f32 v28, v28, s0
	v_fmac_f32_e32 v58, 0xbb000000, v157
	ds_write_b16 v164, v28 offset:10336
	v_mul_f32_e32 v28, v58, v161
	v_fmac_f32_e32 v43, v31, v28
	v_cvt_pk_bf16_f32 v28, v43, s0
	ds_write_b16 v164, v28 offset:10608
	global_load_dwordx4 v[28:31], v160, s[8:9] offset:208
	global_load_dwordx4 v[40:43], v160, s[10:11] offset:208
	v_lshlrev_b32_e32 v56, 16, v24
	v_and_b32_e32 v24, 0xffff0000, v24
	v_fmac_f32_e32 v24, 0xbb000000, v157
	v_mul_f32_e32 v24, v24, v161
	v_lshlrev_b32_e32 v57, 16, v25
	v_fmac_f32_e32 v57, 0xbb000000, v157
	v_and_b32_e32 v25, 0xffff0000, v25
	v_fmac_f32_e32 v56, 0xbb000000, v157
	v_fmac_f32_e32 v25, 0xbb000000, v157
	v_lshlrev_b32_e32 v58, 16, v26
	v_and_b32_e32 v59, 0xffff0000, v26
	v_mul_f32_e32 v26, v56, v161
	v_fmac_f32_e32 v58, 0xbb000000, v157
	v_lshlrev_b32_e32 v60, 16, v27
	v_and_b32_e32 v61, 0xffff0000, v27
	v_fmac_f32_e32 v59, 0xbb000000, v157
	s_waitcnt vmcnt(6)
; #define LAS __attribute__((address_space(3)))
; __device__ __forceinline__ unsigned pk2(float lo, float hi) { f32x2 v = {lo, hi}; bf16x2_t b = __builtin_convertvector(v, bf16x2_t); return __builtin_bit_cast(unsigned, b); }
; __device__ __forceinline__ void cvt8(const u32x4 r, float (&f)[8]) { f[0] = bflo(r.x); f[1] = bfhi(r.x); f[2] = bflo(r.y); f[3] = bfhi(r.y); f[4] = bflo(r.z); f[5] = bfhi(r.z); f[6] = bflo(r.w); f[7] = bfhi(r.w); }
; __device__ __forceinline__ void gmlp_unit(Ctx& C, int l, int uidx) {
;     ...
;         for (int c8 = 0; c8 < 8; ++c8) { float f[8]; cvt8(r2[c8], f);
;             const f32x4 g0 = *(const f32x4*)(lg + 8 * c8), g1 = *(const f32x4*)(lg + 8 * c8 + 4), b0 = *(const f32x4*)(lb + 8 * c8), b1 = *(const f32x4*)(lb + 8 * c8 + 4);
;             const float gg[8] = {g0[0], g0[1], g0[2], g0[3], g1[0], g1[1], g1[2], g1[3]}, bb[8] = {b0[0], b0[1], b0[2], b0[3], b1[0], b1[1], b1[2], b1[3]};
; #pragma unroll
;             for (int j = 0; j < 8; ++j) { const float vn = (f[j] - mean) * rstd * gg[j] + bb[j];
;                 *(LAS bf16*)(C.lds + (64 * part + 8 * c8 + j) * VS + tok * 2) = (bf16)(pk2(vn, 0.f) & 0xffffu); } }
;     }
;     __syncthreads();
	v_fma_f32 v24, v37, v24, v49
	v_cvt_pk_bf16_f32 v24, v24, s0
	ds_write_b16 v164, v24 offset:11152
	v_mul_f32_e32 v24, v57, v161
	v_fma_f32 v24, v38, v24, v50
	v_cvt_pk_bf16_f32 v24, v24, s0
	ds_write_b16 v164, v24 offset:11424
	v_mul_f32_e32 v24, v25, v161
	v_fma_f32 v26, v36, v26, v48
	v_fmac_f32_e32 v51, v39, v24
	v_cvt_pk_bf16_f32 v26, v26, s0
	v_cvt_pk_bf16_f32 v24, v51, s0
	v_mul_f32_e32 v48, v58, v161
	ds_write_b16 v164, v26 offset:10880
	ds_write_b16 v164, v24 offset:11696
	s_waitcnt vmcnt(4)
	v_fma_f32 v16, v16, v48, v44
	global_load_dwordx4 v[24:27], v160, s[8:9] offset:224
	global_load_dwordx4 v[36:39], v160, s[10:11] offset:224
	v_cvt_pk_bf16_f32 v16, v16, s0
	ds_write_b16 v164, v16 offset:11968
	v_mul_f32_e32 v16, v59, v161
	v_fma_f32 v16, v17, v16, v45
	v_cvt_pk_bf16_f32 v16, v16, s0
	v_fmac_f32_e32 v60, 0xbb000000, v157
	ds_write_b16 v164, v16 offset:12240
	v_mul_f32_e32 v16, v60, v161
	v_fma_f32 v16, v18, v16, v46
	v_cvt_pk_bf16_f32 v16, v16, s0
	v_fmac_f32_e32 v61, 0xbb000000, v157
	ds_write_b16 v164, v16 offset:12512
	v_mul_f32_e32 v16, v61, v161
	v_fmac_f32_e32 v47, v19, v16
	v_cvt_pk_bf16_f32 v48, v47, s0
	global_load_dwordx4 v[16:19], v160, s[8:9] offset:240
	global_load_dwordx4 v[44:47], v160, s[10:11] offset:240
	ds_write_b16 v164, v48 offset:12784
	v_lshlrev_b32_e32 v48, 16, v20
	v_and_b32_e32 v20, 0xffff0000, v20
	v_fmac_f32_e32 v20, 0xbb000000, v157
	v_mul_f32_e32 v20, v20, v161
	v_lshlrev_b32_e32 v49, 16, v21
	v_fmac_f32_e32 v49, 0xbb000000, v157
	v_and_b32_e32 v21, 0xffff0000, v21
	v_fmac_f32_e32 v21, 0xbb000000, v157
	v_lshlrev_b32_e32 v50, 16, v22
	v_fmac_f32_e32 v50, 0xbb000000, v157
	v_and_b32_e32 v22, 0xffff0000, v22
	v_fmac_f32_e32 v22, 0xbb000000, v157
	v_lshlrev_b32_e32 v51, 16, v23
	v_fmac_f32_e32 v51, 0xbb000000, v157
	v_and_b32_e32 v23, 0xffff0000, v23
	s_waitcnt vmcnt(6)
	v_fma_f32 v20, v33, v20, v53
	v_cvt_pk_bf16_f32 v20, v20, s0
	ds_write_b16 v164, v20 offset:13328
	v_mul_f32_e32 v20, v49, v161
	v_fma_f32 v20, v34, v20, v54
	v_cvt_pk_bf16_f32 v20, v20, s0
	ds_write_b16 v164, v20 offset:13600
	v_mul_f32_e32 v20, v21, v161
	v_fmac_f32_e32 v55, v35, v20
	v_cvt_pk_bf16_f32 v20, v55, s0
	ds_write_b16 v164, v20 offset:13872
	v_mul_f32_e32 v20, v50, v161
	v_fmac_f32_e32 v23, 0xbb000000, v157
	v_lshlrev_b32_e32 v21, 16, v13
	s_waitcnt vmcnt(4)
	v_fma_f32 v20, v28, v20, v40
	v_cvt_pk_bf16_f32 v20, v20, s0
	ds_write_b16 v164, v20 offset:14144
	v_mul_f32_e32 v20, v22, v161
	v_fma_f32 v20, v29, v20, v41
	v_cvt_pk_bf16_f32 v20, v20, s0
	ds_write_b16 v164, v20 offset:14416
	v_mul_f32_e32 v20, v51, v161
	v_fma_f32 v20, v30, v20, v42
	v_cvt_pk_bf16_f32 v20, v20, s0
	ds_write_b16 v164, v20 offset:14688
	v_mul_f32_e32 v20, v23, v161
	v_fmac_f32_e32 v43, v31, v20
	v_cvt_pk_bf16_f32 v20, v43, s0
	ds_write_b16 v164, v20 offset:14960
	v_lshlrev_b32_e32 v20, 16, v12
	v_and_b32_e32 v12, 0xffff0000, v12
	v_fmac_f32_e32 v12, 0xbb000000, v157
	v_mul_f32_e32 v12, v12, v161
	v_fmac_f32_e32 v21, 0xbb000000, v157
	v_and_b32_e32 v13, 0xffff0000, v13
	v_fmac_f32_e32 v13, 0xbb000000, v157
	v_lshlrev_b32_e32 v22, 16, v14
	v_fmac_f32_e32 v22, 0xbb000000, v157
	v_and_b32_e32 v14, 0xffff0000, v14
	v_fmac_f32_e32 v14, 0xbb000000, v157
	v_lshlrev_b32_e32 v23, 16, v15
	v_fmac_f32_e32 v23, 0xbb000000, v157
	v_and_b32_e32 v15, 0xffff0000, v15
	v_fmac_f32_e32 v15, 0xbb000000, v157
	v_fmac_f32_e32 v48, 0xbb000000, v157
	v_fmac_f32_e32 v20, 0xbb000000, v157
	v_mul_f32_e32 v48, v48, v161
	s_waitcnt vmcnt(2)
	v_fma_f32 v12, v25, v12, v37
	v_cvt_pk_bf16_f32 v12, v12, s0
	ds_write_b16 v164, v12 offset:15504
	v_mul_f32_e32 v12, v21, v161
	v_fma_f32 v12, v26, v12, v38
	v_cvt_pk_bf16_f32 v12, v12, s0
	ds_write_b16 v164, v12 offset:15776
	v_mul_f32_e32 v12, v13, v161
	v_fmac_f32_e32 v39, v27, v12
	v_cvt_pk_bf16_f32 v12, v39, s0
	ds_write_b16 v164, v12 offset:16048
	v_mul_f32_e32 v12, v22, v161
	v_mul_f32_e32 v20, v20, v161
	v_fma_f32 v32, v32, v48, v52
	v_fma_f32 v20, v24, v20, v36
	v_cvt_pk_bf16_f32 v32, v32, s0
	s_waitcnt vmcnt(0)
	v_fma_f32 v12, v16, v12, v44
	v_cvt_pk_bf16_f32 v12, v12, s0
	ds_write_b16 v164, v12 offset:16320
	v_mul_f32_e32 v12, v14, v161
	v_fma_f32 v12, v17, v12, v45
	v_cvt_pk_bf16_f32 v12, v12, s0
	ds_write_b16 v164, v12 offset:16592
	v_mul_f32_e32 v12, v23, v161
	v_fma_f32 v12, v18, v12, v46
	v_cvt_pk_bf16_f32 v12, v12, s0
	ds_write_b16 v164, v12 offset:16864
	v_mul_f32_e32 v12, v15, v161
	v_fmac_f32_e32 v47, v19, v12
	v_cvt_pk_bf16_f32 v12, v47, s0
	ds_write_b16 v164, v12 offset:17136
	v_lshl_or_b32 v12, s19, 6, v159
	v_mul_lo_u32 v12, v12, s6
	v_cvt_pk_bf16_f32 v20, v20, s0
	v_add3_u32 v156, 0, v156, v12
	ds_write_b16 v164, v32 offset:13056
	ds_write_b16 v164, v20 offset:15232
	s_waitcnt lgkmcnt(0)
	s_barrier
; #define LAS __attribute__((address_space(3)))
; __device__ __forceinline__ unsigned pk2(float lo, float hi) { f32x2 v = {lo, hi}; bf16x2_t b = __builtin_convertvector(v, bf16x2_t); return __builtin_bit_cast(unsigned, b); }
; __device__ __forceinline__ float bflo(unsigned w) { return __uint_as_float(w << 16); }
; __device__ __forceinline__ float bfhi(unsigned w) { return __uint_as_float(w & 0xffff0000u); }
; #define MFMA32(a, b, c) __builtin_amdgcn_mfma_f32_32x32x16_bf16((a), (b), (c), 0, 0, 0)
; __device__ __forceinline__ void gmlp_unit(Ctx& C, int l, int uidx) {
;     ...
;     for (int s = 0; s < 8; ++s) {
;         bf16x8 Vf[2];
; #pragma unroll
;         for (int cb = 0; cb < 2; ++cb) Vf[cb] = *(const LAS bf16x8*)(C.lds + (64 * gl + 32 * cb + r32) * VS + (16 * s + 8 * h) * 2);
; #pragma unroll
;         for (int cb = 0; cb < 2; ++cb)
; #pragma unroll
;             for (int pb = 0; pb < 2; ++pb) acc[cb][pb] = MFMA32(Vf[cb], Wf[pb][s], acc[cb][pb]);
;     }
;     bf16* Y = WSP(bf16, WS_YCAT);
; #pragma unroll
;     for (int pb = 0; pb < 2; ++pb) { const int p = 64 * ph + 32 * pb + r32; const float bs = INP(I_GBS)[(l * 8 + g) * 128 + p];
;         bf16* yp = Y + (size_t)(row0 + p) * DM + 1536 + 64 * g + 4 * h;
; #pragma unroll
;         for (int cb = 0; cb < 2; ++cb)
; #pragma unroll
;             for (int rg = 0; rg < 4; ++rg) { const u32x2 uv = upre[pb][cb][rg];
;                 u32x2 w; w.x = pk2(bflo(uv.x) * (acc[cb][pb][4 * rg] + bs), bfhi(uv.x) * (acc[cb][pb][4 * rg + 1] + bs)); w.y = pk2(bflo(uv.y) * (acc[cb][pb][4 * rg + 2] + bs), bfhi(uv.y) * (acc[cb][pb][4 * rg + 3] + bs));
;                 *(u32x2*)(yp + 32 * cb + 8 * rg) = w; } }
	ds_read_b128 v[12:15], v156
	ds_read_b128 v[180:183], v156 offset:32
	s_waitcnt lgkmcnt(1)
	v_mfma_f32_32x32x16_bf16 v[52:67], v[12:15], v[4:7], 0
	s_lshl_b32 s6, s14, 7
	s_mov_b64 s[8:9], 0x3e000c00
	v_mfma_f32_32x32x16_bf16 v[20:35], v[12:15], v[8:11], 0
	ds_read_b128 v[12:15], v156 offset:8704
	ds_read_b128 v[184:187], v156 offset:8736
	s_waitcnt lgkmcnt(1)
	v_mfma_f32_32x32x16_bf16 v[36:51], v[12:15], v[4:7], 0
	v_mfma_f32_32x32x16_bf16 v[4:19], v[12:15], v[8:11], 0
	v_mfma_f32_32x32x16_bf16 v[52:67], v[180:183], v[116:119], v[52:67]
	v_mfma_f32_32x32x16_bf16 v[20:35], v[180:183], v[120:123], v[20:35]
	s_waitcnt lgkmcnt(0)
	v_mfma_f32_32x32x16_bf16 v[36:51], v[184:187], v[116:119], v[36:51]
	v_mfma_f32_32x32x16_bf16 v[4:19], v[184:187], v[120:123], v[4:19]
	ds_read_b128 v[116:119], v156 offset:64
	ds_read_b128 v[120:123], v156 offset:96
	s_waitcnt lgkmcnt(1)
	v_mfma_f32_32x32x16_bf16 v[52:67], v[116:119], v[104:107], v[52:67]
	v_mfma_f32_32x32x16_bf16 v[20:35], v[116:119], v[112:115], v[20:35]
	ds_read_b128 v[116:119], v156 offset:8768
	ds_read_b128 v[180:183], v156 offset:8800
	s_waitcnt lgkmcnt(1)
	v_mfma_f32_32x32x16_bf16 v[36:51], v[116:119], v[104:107], v[36:51]
	v_mfma_f32_32x32x16_bf16 v[4:19], v[116:119], v[112:115], v[4:19]
	v_mfma_f32_32x32x16_bf16 v[52:67], v[120:123], v[100:103], v[52:67]
	v_mfma_f32_32x32x16_bf16 v[20:35], v[120:123], v[108:111], v[20:35]
	s_waitcnt lgkmcnt(0)
	v_mfma_f32_32x32x16_bf16 v[36:51], v[180:183], v[100:103], v[36:51]
	ds_read_b128 v[100:103], v156 offset:128
	ds_read_b128 v[104:107], v156 offset:160
	v_mfma_f32_32x32x16_bf16 v[4:19], v[180:183], v[108:111], v[4:19]
	s_waitcnt lgkmcnt(1)
	v_mfma_f32_32x32x16_bf16 v[52:67], v[100:103], v[88:91], v[52:67]
	v_mfma_f32_32x32x16_bf16 v[20:35], v[100:103], v[96:99], v[20:35]
	ds_read_b128 v[100:103], v156 offset:8832
	ds_read_b128 v[108:111], v156 offset:8864
	s_waitcnt lgkmcnt(1)
	v_mfma_f32_32x32x16_bf16 v[36:51], v[100:103], v[88:91], v[36:51]
	v_mfma_f32_32x32x16_bf16 v[4:19], v[100:103], v[96:99], v[4:19]
	v_mfma_f32_32x32x16_bf16 v[52:67], v[104:107], v[84:87], v[52:67]
	v_mfma_f32_32x32x16_bf16 v[20:35], v[104:107], v[92:95], v[20:35]
	s_waitcnt lgkmcnt(0)
	v_mfma_f32_32x32x16_bf16 v[36:51], v[108:111], v[84:87], v[36:51]
	ds_read_b128 v[84:87], v156 offset:192
	ds_read_b128 v[88:91], v156 offset:224
	v_mfma_f32_32x32x16_bf16 v[4:19], v[108:111], v[92:95], v[4:19]
	s_waitcnt lgkmcnt(1)
	v_mfma_f32_32x32x16_bf16 v[52:67], v[84:87], v[76:79], v[52:67]
	v_mfma_f32_32x32x16_bf16 v[20:35], v[84:87], v[80:83], v[20:35]
	ds_read_b128 v[84:87], v156 offset:8896
	ds_read_b128 v[92:95], v156 offset:8928
	s_waitcnt lgkmcnt(1)
	v_mfma_f32_32x32x16_bf16 v[4:19], v[84:87], v[80:83], v[4:19]
	v_or_b32_e32 v80, s15, v159
	v_lshlrev_b32_e32 v82, 16, v154
	v_and_b32_e32 v83, 0xffff0000, v154
	v_mfma_f32_32x32x16_bf16 v[36:51], v[84:87], v[76:79], v[36:51]
	v_or_b32_e32 v76, s6, v80
	v_ashrrev_i32_e32 v77, 31, v76
	v_lshl_add_u64 v[78:79], v[76:77], 2, s[58:59]
	global_load_dword v244, v[78:79], off offset:128
	global_load_dword v78, v[78:79], off
	s_ashr_i32 s6, s6, 31
	v_mov_b32_e32 v77, s6
	v_mfma_f32_32x32x16_bf16 v[52:67], v[88:91], v[72:75], v[52:67]
	s_waitcnt lgkmcnt(0)
	v_mfma_f32_32x32x16_bf16 v[36:51], v[92:95], v[72:75], v[36:51]
	v_or_b32_e32 v72, s18, v80
	v_lshlrev_b32_e32 v72, 12, v72
	v_mov_b32_e32 v73, v3
	v_lshl_add_u64 v[74:75], s[54:55], 0, v[72:73]
	v_lshl_add_u64 v[74:75], v[74:75], 0, s[12:13]
	v_lshl_add_u64 v[74:75], v[74:75], 0, v[2:3]
	v_lshl_add_u64 v[80:81], v[74:75], 0, s[8:9]
	v_mfma_f32_32x32x16_bf16 v[20:35], v[88:91], v[68:71], v[20:35]
	s_waitcnt vmcnt(0)
	s_nop 0
	v_add_f32_e64 v52, v52, v78
	v_add_f32_e64 v53, v53, v78
	v_mul_f32_e64 v52, v52, v82
	v_mul_f32_e64 v53, v53, v83
	v_lshlrev_b32_e32 v82, 16, v155
	v_and_b32_e32 v83, 0xffff0000, v155
	v_pk_add_f32 v[54:55], v[54:55], v[78:79] op_sel_hi:[1,0]
	v_cvt_pk_bf16_f32 v52, v52, v53
	v_pk_mul_f32 v[54:55], v[54:55], v[82:83]
	v_pk_add_f32 v[36:37], v[36:37], v[78:79] op_sel_hi:[1,0]
	v_cvt_pk_bf16_f32 v53, v54, v55
	v_add_co_u32_e32 v54, vcc, s73, v74
	v_pk_add_f32 v[38:39], v[38:39], v[78:79] op_sel_hi:[1,0]
	s_nop 0
	v_addc_co_u32_e32 v55, vcc, 0, v75, vcc
	global_store_dwordx2 v[54:55], v[52:53], off offset:3072
	v_lshlrev_b32_e32 v52, 16, v152
	v_and_b32_e32 v53, 0xffff0000, v152
	v_pk_add_f32 v[54:55], v[56:57], v[78:79] op_sel_hi:[1,0]
	v_pk_add_f32 v[56:57], v[58:59], v[78:79] op_sel_hi:[1,0]
	v_pk_mul_f32 v[52:53], v[54:55], v[52:53]
	v_lshlrev_b32_e32 v54, 16, v153
	v_and_b32_e32 v55, 0xffff0000, v153
	v_pk_mul_f32 v[54:55], v[56:57], v[54:55]
	v_cvt_pk_bf16_f32 v52, v52, v53
	v_cvt_pk_bf16_f32 v53, v54, v55
	global_store_dwordx2 v[80:81], v[52:53], off offset:16
	v_lshlrev_b32_e32 v52, 16, v150
	v_and_b32_e32 v53, 0xffff0000, v150
	v_pk_add_f32 v[54:55], v[60:61], v[78:79] op_sel_hi:[1,0]
	v_pk_add_f32 v[56:57], v[62:63], v[78:79] op_sel_hi:[1,0]
	v_pk_mul_f32 v[52:53], v[54:55], v[52:53]
	v_lshlrev_b32_e32 v54, 16, v151
	v_and_b32_e32 v55, 0xffff0000, v151
	v_pk_mul_f32 v[54:55], v[56:57], v[54:55]
	v_cvt_pk_bf16_f32 v52, v52, v53
	v_cvt_pk_bf16_f32 v53, v54, v55
	global_store_dwordx2 v[80:81], v[52:53], off offset:32
	v_lshlrev_b32_e32 v52, 16, v148
	v_and_b32_e32 v53, 0xffff0000, v148
	v_pk_add_f32 v[54:55], v[64:65], v[78:79] op_sel_hi:[1,0]
	v_pk_add_f32 v[56:57], v[66:67], v[78:79] op_sel_hi:[1,0]
	v_pk_mul_f32 v[52:53], v[54:55], v[52:53]
	v_lshlrev_b32_e32 v54, 16, v149
	v_and_b32_e32 v55, 0xffff0000, v149
	v_pk_mul_f32 v[54:55], v[56:57], v[54:55]
	v_cvt_pk_bf16_f32 v52, v52, v53
	v_cvt_pk_bf16_f32 v53, v54, v55
	global_store_dwordx2 v[80:81], v[52:53], off offset:48
; __device__ __forceinline__ unsigned pk2(float lo, float hi) { f32x2 v = {lo, hi}; bf16x2_t b = __builtin_convertvector(v, bf16x2_t); return __builtin_bit_cast(unsigned, b); }
; __device__ __forceinline__ float bflo(unsigned w) { return __uint_as_float(w << 16); }
; __device__ __forceinline__ float bfhi(unsigned w) { return __uint_as_float(w & 0xffff0000u); }
; __device__ __forceinline__ void gmlp_unit(Ctx& C, int l, int uidx) {
;     ...
;     for (int pb = 0; pb < 2; ++pb) { const int p = 64 * ph + 32 * pb + r32; const float bs = INP(I_GBS)[(l * 8 + g) * 128 + p];
;         bf16* yp = Y + (size_t)(row0 + p) * DM + 1536 + 64 * g + 4 * h;
; #pragma unroll
;         for (int cb = 0; cb < 2; ++cb)
; #pragma unroll
;             for (int rg = 0; rg < 4; ++rg) { const u32x2 uv = upre[pb][cb][rg];
;                 u32x2 w; w.x = pk2(bflo(uv.x) * (acc[cb][pb][4 * rg] + bs), bfhi(uv.x) * (acc[cb][pb][4 * rg + 1] + bs)); w.y = pk2(bflo(uv.y) * (acc[cb][pb][4 * rg + 2] + bs), bfhi(uv.y) * (acc[cb][pb][4 * rg + 3] + bs));
;                 *(u32x2*)(yp + 32 * cb + 8 * rg) = w; } }
	v_lshlrev_b32_e32 v52, 16, v146
	v_and_b32_e32 v53, 0xffff0000, v146
	v_pk_mul_f32 v[36:37], v[36:37], v[52:53]
	v_lshlrev_b32_e32 v52, 16, v147
	v_and_b32_e32 v53, 0xffff0000, v147
	v_pk_mul_f32 v[38:39], v[38:39], v[52:53]
	v_cvt_pk_bf16_f32 v36, v36, v37
	v_cvt_pk_bf16_f32 v37, v38, v39
	global_store_dwordx2 v[80:81], v[36:37], off offset:64
	v_lshlrev_b32_e32 v36, 16, v144
	v_and_b32_e32 v37, 0xffff0000, v144
	v_pk_add_f32 v[38:39], v[40:41], v[78:79] op_sel_hi:[1,0]
	v_pk_add_f32 v[40:41], v[42:43], v[78:79] op_sel_hi:[1,0]
	v_pk_mul_f32 v[36:37], v[38:39], v[36:37]
	v_lshlrev_b32_e32 v38, 16, v145
	v_and_b32_e32 v39, 0xffff0000, v145
	v_pk_mul_f32 v[38:39], v[40:41], v[38:39]
	v_cvt_pk_bf16_f32 v36, v36, v37
	v_cvt_pk_bf16_f32 v37, v38, v39
	global_store_dwordx2 v[80:81], v[36:37], off offset:80
	v_lshlrev_b32_e32 v36, 16, v142
	v_and_b32_e32 v37, 0xffff0000, v142
	v_pk_add_f32 v[38:39], v[44:45], v[78:79] op_sel_hi:[1,0]
	v_pk_add_f32 v[40:41], v[46:47], v[78:79] op_sel_hi:[1,0]
	v_pk_mul_f32 v[36:37], v[38:39], v[36:37]
	v_lshlrev_b32_e32 v38, 16, v143
	v_and_b32_e32 v39, 0xffff0000, v143
	v_pk_mul_f32 v[38:39], v[40:41], v[38:39]
	v_cvt_pk_bf16_f32 v36, v36, v37
	v_cvt_pk_bf16_f32 v37, v38, v39
	global_store_dwordx2 v[80:81], v[36:37], off offset:96
	v_lshlrev_b32_e32 v36, 16, v140
	v_and_b32_e32 v37, 0xffff0000, v140
	v_pk_add_f32 v[38:39], v[48:49], v[78:79] op_sel_hi:[1,0]
	v_pk_add_f32 v[40:41], v[50:51], v[78:79] op_sel_hi:[1,0]
	v_pk_mul_f32 v[36:37], v[38:39], v[36:37]
	v_lshlrev_b32_e32 v38, 16, v141
	v_and_b32_e32 v39, 0xffff0000, v141
	v_pk_mul_f32 v[38:39], v[40:41], v[38:39]
	v_cvt_pk_bf16_f32 v36, v36, v37
	v_cvt_pk_bf16_f32 v37, v38, v39
	global_store_dwordx2 v[80:81], v[36:37], off offset:112
	v_mov_b32_e32 v36, v244
	v_or_b32_e32 v38, 0x20000, v72
	v_mov_b32_e32 v39, v3
	v_lshl_add_u64 v[38:39], s[54:55], 0, v[38:39]
	v_lshlrev_b32_e32 v42, 16, v138
	v_and_b32_e32 v43, 0xffff0000, v138
	v_lshl_add_u64 v[38:39], v[38:39], 0, s[12:13]
	v_lshl_add_u64 v[38:39], v[38:39], 0, v[2:3]
	v_lshl_add_u64 v[40:41], v[38:39], 0, s[8:9]
	v_mfma_f32_32x32x16_bf16 v[4:19], v[92:95], v[68:71], v[4:19]
	v_add_f32_e64 v20, v20, v36
	v_add_f32_e64 v21, v21, v36
	v_mul_f32_e64 v20, v20, v42
	v_mul_f32_e64 v21, v21, v43
	v_lshlrev_b32_e32 v42, 16, v139
	v_and_b32_e32 v43, 0xffff0000, v139
	v_pk_add_f32 v[22:23], v[22:23], v[36:37] op_sel_hi:[1,0]
	v_cvt_pk_bf16_f32 v20, v20, v21
	v_pk_mul_f32 v[22:23], v[22:23], v[42:43]
	s_nop 1
	v_pk_add_f32 v[4:5], v[4:5], v[36:37] op_sel_hi:[1,0]
	v_cvt_pk_bf16_f32 v21, v22, v23
	v_add_co_u32_e32 v22, vcc, s73, v38
	v_pk_add_f32 v[6:7], v[6:7], v[36:37] op_sel_hi:[1,0]
	s_nop 0
	v_addc_co_u32_e32 v23, vcc, 0, v39, vcc
	global_store_dwordx2 v[22:23], v[20:21], off offset:3072
	v_lshlrev_b32_e32 v20, 16, v136
	v_and_b32_e32 v21, 0xffff0000, v136
	v_pk_add_f32 v[22:23], v[24:25], v[36:37] op_sel_hi:[1,0]
	v_pk_add_f32 v[24:25], v[26:27], v[36:37] op_sel_hi:[1,0]
	v_pk_mul_f32 v[20:21], v[22:23], v[20:21]
	v_lshlrev_b32_e32 v22, 16, v137
	v_and_b32_e32 v23, 0xffff0000, v137
	v_pk_mul_f32 v[22:23], v[24:25], v[22:23]
	v_cvt_pk_bf16_f32 v20, v20, v21
	v_cvt_pk_bf16_f32 v21, v22, v23
	global_store_dwordx2 v[40:41], v[20:21], off offset:16
	v_lshlrev_b32_e32 v20, 16, v134
	v_and_b32_e32 v21, 0xffff0000, v134
	v_pk_add_f32 v[22:23], v[28:29], v[36:37] op_sel_hi:[1,0]
	v_pk_add_f32 v[24:25], v[30:31], v[36:37] op_sel_hi:[1,0]
	v_pk_mul_f32 v[20:21], v[22:23], v[20:21]
	v_lshlrev_b32_e32 v22, 16, v135
	v_and_b32_e32 v23, 0xffff0000, v135
	v_pk_mul_f32 v[22:23], v[24:25], v[22:23]
	v_cvt_pk_bf16_f32 v20, v20, v21
	v_cvt_pk_bf16_f32 v21, v22, v23
	global_store_dwordx2 v[40:41], v[20:21], off offset:32
	v_lshlrev_b32_e32 v20, 16, v132
	v_and_b32_e32 v21, 0xffff0000, v132
	v_pk_add_f32 v[22:23], v[32:33], v[36:37] op_sel_hi:[1,0]
	v_pk_add_f32 v[24:25], v[34:35], v[36:37] op_sel_hi:[1,0]
	v_pk_mul_f32 v[20:21], v[22:23], v[20:21]
	v_lshlrev_b32_e32 v22, 16, v133
	v_and_b32_e32 v23, 0xffff0000, v133
	v_pk_mul_f32 v[22:23], v[24:25], v[22:23]
	v_cvt_pk_bf16_f32 v20, v20, v21
	v_cvt_pk_bf16_f32 v21, v22, v23
	global_store_dwordx2 v[40:41], v[20:21], off offset:48
	v_lshlrev_b32_e32 v20, 16, v130
	v_and_b32_e32 v21, 0xffff0000, v130
	v_pk_mul_f32 v[4:5], v[4:5], v[20:21]
	v_lshlrev_b32_e32 v20, 16, v131
	v_and_b32_e32 v21, 0xffff0000, v131
	v_pk_mul_f32 v[6:7], v[6:7], v[20:21]
	v_cvt_pk_bf16_f32 v4, v4, v5
	v_cvt_pk_bf16_f32 v5, v6, v7
	global_store_dwordx2 v[40:41], v[4:5], off offset:64
	v_lshlrev_b32_e32 v4, 16, v128
	v_and_b32_e32 v5, 0xffff0000, v128
	v_pk_add_f32 v[6:7], v[8:9], v[36:37] op_sel_hi:[1,0]
	v_pk_add_f32 v[8:9], v[10:11], v[36:37] op_sel_hi:[1,0]
	v_pk_mul_f32 v[4:5], v[6:7], v[4:5]
	v_lshlrev_b32_e32 v6, 16, v129
	v_and_b32_e32 v7, 0xffff0000, v129
	v_pk_mul_f32 v[6:7], v[8:9], v[6:7]
	v_cvt_pk_bf16_f32 v4, v4, v5
	v_cvt_pk_bf16_f32 v5, v6, v7
	global_store_dwordx2 v[40:41], v[4:5], off offset:80
	v_lshlrev_b32_e32 v4, 16, v126
	v_and_b32_e32 v5, 0xffff0000, v126
	v_pk_add_f32 v[6:7], v[12:13], v[36:37] op_sel_hi:[1,0]
	v_pk_add_f32 v[8:9], v[14:15], v[36:37] op_sel_hi:[1,0]
	v_pk_mul_f32 v[4:5], v[6:7], v[4:5]
	v_lshlrev_b32_e32 v6, 16, v127
	v_and_b32_e32 v7, 0xffff0000, v127
	v_pk_mul_f32 v[6:7], v[8:9], v[6:7]
	v_cvt_pk_bf16_f32 v4, v4, v5
	v_cvt_pk_bf16_f32 v5, v6, v7
	global_store_dwordx2 v[40:41], v[4:5], off offset:96
	v_lshlrev_b32_e32 v4, 16, v124
	v_and_b32_e32 v5, 0xffff0000, v124
	v_pk_add_f32 v[6:7], v[16:17], v[36:37] op_sel_hi:[1,0]
	v_pk_add_f32 v[8:9], v[18:19], v[36:37] op_sel_hi:[1,0]
	v_pk_mul_f32 v[4:5], v[6:7], v[4:5]
	v_lshlrev_b32_e32 v6, 16, v125
	v_and_b32_e32 v7, 0xffff0000, v125
	v_pk_mul_f32 v[6:7], v[8:9], v[6:7]
	v_cvt_pk_bf16_f32 v4, v4, v5
	v_cvt_pk_bf16_f32 v5, v6, v7
	global_store_dwordx2 v[40:41], v[4:5], off offset:112

; __device__ __forceinline__ void gmlp_unit(Ctx& C, int l, int uidx) {
;     ...
;     const int ck = uidx >> 1, hf = uidx & 1, row0 = 128 * ck;
;     const bf16* Z = WSP(bf16, WS_Z);
;     const int gl = C.wave >> 1, ph = C.wave & 1, g = 4 * hf + gl, r32 = C.lane & 31, h = C.lane >> 5;
;     bf16x8 Wf[2][8]; u32x2 upre[2][2][4];
;     { const bf16* wsb = WSP(bf16, WS_GWSB) + ((size_t)(l * 8 + g) * 128 + 64 * ph + r32) * 128 + 8 * h;
; #pragma unroll
;       for (int pb = 0; pb < 2; ++pb)
; #pragma unroll
;           for (int s = 0; s < 8; ++s) Wf[pb][s] = *(const bf16x8*)(wsb + (size_t)(32 * pb) * 128 + 16 * s);
; #pragma unroll
;       for (int pb = 0; pb < 2; ++pb) { const bf16* up = Z + (size_t)(row0 + 64 * ph + 32 * pb + r32) * INW + 2816 + 64 * g + 4 * h;
; #pragma unroll
;           for (int cb = 0; cb < 2; ++cb)
; #pragma unroll
;               for (int rg = 0; rg < 4; ++rg) upre[pb][cb][rg] = *(const u32x2*)(up + 32 * cb + 8 * rg); } }
;     __syncthreads();
;     {
;         const int tok = C.tid >> 2, part = C.tid & 3;
;         const bf16* zp = Z + (size_t)(row0 + tok) * INW + 3328 + 128 * part;
;         const bf16* zq = Z + (size_t)(row0 + tok) * INW + 3328 + 256 * hf + 64 * part;
;         u32x4 r1[16], r2[8];
; #pragma unroll
;         for (int c8 = 0; c8 < 16; ++c8) r1[c8] = *(const u32x4*)(zp + 8 * c8);
; #pragma unroll
;         for (int c8 = 0; c8 < 8; ++c8) r2[c8] = *(const u32x4*)(zq + 8 * c8);
.LBB0_1732:
	s_andn2_b64 vcc, exec, s[6:7]
	s_cbranch_vccnz .LBB0_1734
	s_and_b32 s6, s56, 1
	s_ashr_i32 s34, s57, 7
	s_lshl_b32 s8, s6, 2
	s_add_i32 s10, s34, s8
	s_add_i32 s52, s10, 8
	s_ashr_i32 s53, s52, 31
	s_lshl_b64 s[8:9], s[52:53], 7
	s_and_b32 s18, s57, 64
	v_and_b32_e32 v161, 31, v172
	s_or_b32 s8, s8, s18
	v_or_b32_e32 v4, s8, v161
	v_mov_b32_e32 v5, s9
	v_lshrrev_b32_e32 v6, 5, v160
	v_lshlrev_b64 v[4:5], 8, v[4:5]
	v_lshl_add_u64 v[4:5], s[46:47], 0, v[4:5]
	v_lshlrev_b32_e32 v156, 4, v6
	v_mov_b32_e32 v157, v3
	v_lshl_add_u64 v[8:9], v[4:5], 0, v[156:157]
	s_mov_b64 s[8:9], 0x380000
	s_lshl_b32 s7, s56, 6
	v_lshl_add_u64 v[10:11], v[8:9], 0, s[8:9]
	s_mov_b32 s8, 0x380000
	v_add_co_u32_e32 v4, vcc, s8, v8
	s_and_b32 s7, s7, 0x7f80
	s_nop 0
	v_addc_co_u32_e32 v5, vcc, 0, v9, vcc
	s_mov_b32 s8, 0x382000
	s_xor_b32 s19, s7, 0x4000
	v_add_co_u32_e32 v12, vcc, s8, v8
	s_add_u32 s8, s46, 0x36000000
	s_nop 0
	v_addc_co_u32_e32 v13, vcc, 0, v9, vcc
	s_addc_u32 s9, s47, 0
	s_or_b32 s7, s19, s18
	v_lshlrev_b32_e32 v2, 3, v6
	global_load_dwordx4 v[116:119], v[10:11], off offset:32
	global_load_dwordx4 v[104:107], v[10:11], off offset:64
	global_load_dwordx4 v[100:103], v[10:11], off offset:96
	global_load_dwordx4 v[88:91], v[10:11], off offset:128
	global_load_dwordx4 v[84:87], v[10:11], off offset:160
	global_load_dwordx4 v[76:79], v[10:11], off offset:192
	s_nop 0
	global_load_dwordx4 v[4:7], v[4:5], off
	s_nop 0
	global_load_dwordx4 v[72:75], v[10:11], off offset:224
	s_nop 0
	global_load_dwordx4 v[8:11], v[12:13], off
	global_load_dwordx4 v[120:123], v[12:13], off offset:32
	global_load_dwordx4 v[112:115], v[12:13], off offset:64
	global_load_dwordx4 v[108:111], v[12:13], off offset:96
	global_load_dwordx4 v[96:99], v[12:13], off offset:128
	global_load_dwordx4 v[92:95], v[12:13], off offset:160
	global_load_dwordx4 v[80:83], v[12:13], off offset:192
	global_load_dwordx4 v[68:71], v[12:13], off offset:224
	v_or_b32_e32 v12, s7, v161
	s_lshl_b32 s10, s10, 6
	v_mul_u32_u24_e32 v12, 0xf00, v12
	s_ashr_i32 s11, s10, 31
	v_lshlrev_b32_e32 v12, 1, v12
	v_mov_b32_e32 v13, v3
	v_lshl_add_u64 v[12:13], s[8:9], 0, v[12:13]
	s_lshl_b64 s[50:51], s[10:11], 1
	v_lshl_add_u64 v[12:13], v[12:13], 0, s[50:51]
	v_lshl_add_u64 v[12:13], v[12:13], 0, v[2:3]
	s_mov_b64 s[10:11], 0x1600
	v_add_co_u32_e32 v16, vcc, s62, v12
	v_lshl_add_u64 v[14:15], v[12:13], 0, s[10:11]
	s_nop 0
	v_addc_co_u32_e32 v17, vcc, 0, v13, vcc
	s_mov_b64 s[10:11], 0x3d600
	s_mov_b32 s7, 0x3d000
	global_load_dwordx2 v[152:153], v[14:15], off offset:16
	global_load_dwordx2 v[150:151], v[14:15], off offset:32
	global_load_dwordx2 v[148:149], v[14:15], off offset:48
	global_load_dwordx2 v[146:147], v[14:15], off offset:64
	global_load_dwordx2 v[154:155], v[16:17], off offset:1536
	global_load_dwordx2 v[144:145], v[14:15], off offset:80
	global_load_dwordx2 v[142:143], v[14:15], off offset:96
	global_load_dwordx2 v[140:141], v[14:15], off offset:112
	v_lshl_add_u64 v[14:15], v[12:13], 0, s[10:11]
	v_add_co_u32_e32 v12, vcc, s7, v12
	v_ashrrev_i32_e32 v62, 2, v172
	s_nop 0
	v_addc_co_u32_e32 v13, vcc, 0, v13, vcc
	global_load_dwordx2 v[136:137], v[14:15], off offset:16
	global_load_dwordx2 v[134:135], v[14:15], off offset:32
	global_load_dwordx2 v[132:133], v[14:15], off offset:48
	global_load_dwordx2 v[130:131], v[14:15], off offset:64
	global_load_dwordx2 v[138:139], v[12:13], off offset:1536
	global_load_dwordx2 v[128:129], v[14:15], off offset:80
	global_load_dwordx2 v[126:127], v[14:15], off offset:96
	global_load_dwordx2 v[124:125], v[14:15], off offset:112
	v_add_u32_e32 v14, s19, v62
	v_mov_b64_e32 v[12:13], s[8:9]
	v_mad_i64_i32 v[12:13], s[8:9], v14, s63, v[12:13]
	v_and_b32_e32 v162, 3, v172
	s_mov_b64 s[8:9], 0x1a00
	v_lshl_add_u64 v[16:17], v[12:13], 0, s[8:9]
	v_lshlrev_b32_e32 v158, 8, v162
	v_mov_b32_e32 v159, v3
	v_lshl_add_u64 v[18:19], v[16:17], 0, v[158:159]
	s_waitcnt lgkmcnt(0)
	s_barrier
	global_load_dwordx4 v[56:59], v[18:19], off
	global_load_dwordx4 v[64:67], v[18:19], off offset:16
	global_load_dwordx4 v[174:177], v[18:19], off offset:32
	global_load_dwordx4 v[178:181], v[18:19], off offset:48
	global_load_dwordx4 v[52:55], v[18:19], off offset:112
	global_load_dwordx4 v[182:185], v[18:19], off offset:96
	global_load_dwordx4 v[186:189], v[18:19], off offset:80
	global_load_dwordx4 v[190:193], v[18:19], off offset:64
	global_load_dwordx4 v[36:39], v[18:19], off offset:176
	global_load_dwordx4 v[40:43], v[18:19], off offset:160
	global_load_dwordx4 v[44:47], v[18:19], off offset:144
	global_load_dwordx4 v[48:51], v[18:19], off offset:128
	global_load_dwordx4 v[12:15], v[18:19], off offset:240
	global_load_dwordx4 v[20:23], v[18:19], off offset:224
	global_load_dwordx4 v[24:27], v[18:19], off offset:208
	global_load_dwordx4 v[32:35], v[18:19], off offset:192
	s_lshl_b32 s26, s6, 9
	v_lshlrev_b32_e32 v28, 7, v162
	v_mov_b32_e32 v29, v3
	v_lshl_add_u64 v[16:17], v[16:17], 0, s[26:27]
	v_lshl_add_u64 v[60:61], v[16:17], 0, v[28:29]
	global_load_dwordx4 v[16:19], v[60:61], off offset:16
	global_load_dwordx4 v[28:31], v[60:61], off
	s_load_dwordx4 s[8:11], s[48:49], 0xb0
	s_load_dwordx2 s[54:55], s[48:49], 0xc8
	s_lshl_b32 s6, s6, 10
	v_mul_u32_u24_e32 v162, 0x4400, v162
	s_waitcnt lgkmcnt(0)
	s_add_u32 s8, s8, s6
	s_addc_u32 s9, s9, 0
	s_add_u32 s10, s10, s6
	s_addc_u32 s11, s11, 0
	s_mov_b32 s6, 0x3b000000
	s_waitcnt vmcnt(17)
; __device__ __forceinline__ void cvt8(const u32x4 r, float (&f)[8]) { f[0] = bflo(r.x); f[1] = bfhi(r.x); f[2] = bflo(r.y); f[3] = bfhi(r.y); f[4] = bflo(r.z); f[5] = bfhi(r.z); f[6] = bflo(r.w); f[7] = bfhi(r.w); }
; __device__ __forceinline__ void gmlp_unit(Ctx& C, int l, int uidx) {
;     ...
;         float s = 0.f, q = 0.f;
; #pragma unroll
;         for (int c8 = 0; c8 < 16; ++c8) { float f[8]; cvt8(r1[c8], f);
; #pragma unroll
;             for (int j = 0; j < 8; ++j) { s += f[j]; q += f[j] * f[j]; } }
	v_lshlrev_b32_e32 v63, 16, v56
	v_and_b32_e32 v56, 0xffff0000, v56
	v_add_f32_e32 v173, 0, v63
	v_lshlrev_b32_e32 v157, 16, v57
	v_add_f32_e32 v173, v173, v56
	v_mul_f32_e32 v56, v56, v56
	v_and_b32_e32 v57, 0xffff0000, v57
	v_fmac_f32_e32 v56, v63, v63
	v_add_f32_e32 v63, v173, v157
	v_lshlrev_b32_e32 v159, 16, v58
	v_fmac_f32_e32 v56, v157, v157
	v_add_f32_e32 v63, v63, v57
	v_and_b32_e32 v58, 0xffff0000, v58
	v_fmac_f32_e32 v56, v57, v57
	v_add_f32_e32 v57, v63, v159
	v_lshlrev_b32_e32 v164, 16, v59
	v_fmac_f32_e32 v56, v159, v159
	v_add_f32_e32 v57, v57, v58
	v_and_b32_e32 v59, 0xffff0000, v59
	v_fmac_f32_e32 v56, v58, v58
	v_add_f32_e32 v57, v57, v164
	v_fmac_f32_e32 v56, v164, v164
	v_add_f32_e32 v57, v57, v59
	s_waitcnt vmcnt(16)
	v_lshlrev_b32_e32 v58, 16, v64
	v_fmac_f32_e32 v56, v59, v59
	v_and_b32_e32 v59, 0xffff0000, v64
	v_add_f32_e32 v57, v57, v58
	v_lshlrev_b32_e32 v63, 16, v65
	v_fmac_f32_e32 v56, v58, v58
	v_add_f32_e32 v57, v57, v59
	v_and_b32_e32 v64, 0xffff0000, v65
	v_fmac_f32_e32 v56, v59, v59
	v_add_f32_e32 v57, v57, v63
	v_lshlrev_b32_e32 v65, 16, v66
	v_fmac_f32_e32 v56, v63, v63
	v_add_f32_e32 v57, v57, v64
	v_and_b32_e32 v66, 0xffff0000, v66
	v_fmac_f32_e32 v56, v64, v64
	v_add_f32_e32 v57, v57, v65
	v_lshlrev_b32_e32 v157, 16, v67
	v_fmac_f32_e32 v56, v65, v65
	v_add_f32_e32 v57, v57, v66
	v_and_b32_e32 v67, 0xffff0000, v67
	v_fmac_f32_e32 v56, v66, v66
	v_add_f32_e32 v57, v57, v157
	v_fmac_f32_e32 v56, v157, v157
	v_add_f32_e32 v57, v57, v67
	s_waitcnt vmcnt(15)
	v_lshlrev_b32_e32 v58, 16, v174
	v_fmac_f32_e32 v56, v67, v67
	v_and_b32_e32 v59, 0xffff0000, v174
	v_add_f32_e32 v57, v57, v58
	v_lshlrev_b32_e32 v63, 16, v175
	v_fmac_f32_e32 v56, v58, v58
	v_add_f32_e32 v57, v57, v59
	v_and_b32_e32 v64, 0xffff0000, v175
	v_fmac_f32_e32 v56, v59, v59
	v_add_f32_e32 v57, v57, v63
	v_lshlrev_b32_e32 v65, 16, v176
	v_fmac_f32_e32 v56, v63, v63
	v_add_f32_e32 v57, v57, v64
	v_and_b32_e32 v66, 0xffff0000, v176
	v_fmac_f32_e32 v56, v64, v64
	v_add_f32_e32 v57, v57, v65
	v_lshlrev_b32_e32 v67, 16, v177
	v_fmac_f32_e32 v56, v65, v65
	v_add_f32_e32 v57, v57, v66
	v_and_b32_e32 v157, 0xffff0000, v177
	v_fmac_f32_e32 v56, v66, v66
	v_add_f32_e32 v57, v57, v67
	v_fmac_f32_e32 v56, v67, v67
	v_add_f32_e32 v57, v57, v157
	s_waitcnt vmcnt(14)
	v_lshlrev_b32_e32 v58, 16, v178
	v_fmac_f32_e32 v56, v157, v157
	v_and_b32_e32 v59, 0xffff0000, v178
	v_add_f32_e32 v57, v57, v58
	v_lshlrev_b32_e32 v63, 16, v179
	v_fmac_f32_e32 v56, v58, v58
	v_add_f32_e32 v57, v57, v59
	v_and_b32_e32 v64, 0xffff0000, v179
	v_fmac_f32_e32 v56, v59, v59
	v_add_f32_e32 v57, v57, v63
	v_lshlrev_b32_e32 v65, 16, v180
	v_fmac_f32_e32 v56, v63, v63
	v_add_f32_e32 v57, v57, v64
	v_and_b32_e32 v66, 0xffff0000, v180
	v_fmac_f32_e32 v56, v64, v64
	v_add_f32_e32 v57, v57, v65
	v_lshlrev_b32_e32 v67, 16, v181
	v_fmac_f32_e32 v56, v65, v65
	v_add_f32_e32 v57, v57, v66
	v_and_b32_e32 v157, 0xffff0000, v181
	v_fmac_f32_e32 v56, v66, v66
	v_add_f32_e32 v57, v57, v67
	v_fmac_f32_e32 v56, v67, v67
	v_add_f32_e32 v57, v57, v157
	s_waitcnt vmcnt(10)
	v_lshlrev_b32_e32 v58, 16, v190
	v_fmac_f32_e32 v56, v157, v157
	v_and_b32_e32 v59, 0xffff0000, v190
	v_add_f32_e32 v57, v57, v58
	v_lshlrev_b32_e32 v63, 16, v191
	v_fmac_f32_e32 v56, v58, v58
	v_add_f32_e32 v57, v57, v59
	v_and_b32_e32 v64, 0xffff0000, v191
	v_fmac_f32_e32 v56, v59, v59
	v_add_f32_e32 v57, v57, v63
	v_lshlrev_b32_e32 v65, 16, v192
	v_fmac_f32_e32 v56, v63, v63
	v_add_f32_e32 v57, v57, v64
	v_and_b32_e32 v66, 0xffff0000, v192
	v_fmac_f32_e32 v56, v64, v64
	v_add_f32_e32 v57, v57, v65
	v_lshlrev_b32_e32 v67, 16, v193
	v_fmac_f32_e32 v56, v65, v65
	v_add_f32_e32 v57, v57, v66
	v_and_b32_e32 v157, 0xffff0000, v193
	v_fmac_f32_e32 v56, v66, v66
	v_add_f32_e32 v57, v57, v67
	v_fmac_f32_e32 v56, v67, v67
	v_add_f32_e32 v57, v57, v157
	v_lshlrev_b32_e32 v58, 16, v186
	v_fmac_f32_e32 v56, v157, v157
	v_and_b32_e32 v59, 0xffff0000, v186
	v_add_f32_e32 v57, v57, v58
	v_lshlrev_b32_e32 v63, 16, v187
	v_fmac_f32_e32 v56, v58, v58
	v_add_f32_e32 v57, v57, v59
	v_and_b32_e32 v64, 0xffff0000, v187
	v_fmac_f32_e32 v56, v59, v59
	v_add_f32_e32 v57, v57, v63
	v_lshlrev_b32_e32 v65, 16, v188
	v_fmac_f32_e32 v56, v63, v63
	v_add_f32_e32 v57, v57, v64
	v_and_b32_e32 v66, 0xffff0000, v188
	v_fmac_f32_e32 v56, v64, v64
	v_add_f32_e32 v57, v57, v65
	v_lshlrev_b32_e32 v67, 16, v189
	v_fmac_f32_e32 v56, v65, v65
	v_add_f32_e32 v57, v57, v66
	v_and_b32_e32 v157, 0xffff0000, v189
	v_fmac_f32_e32 v56, v66, v66
	v_add_f32_e32 v57, v57, v67
	v_fmac_f32_e32 v56, v67, v67
	v_add_f32_e32 v57, v57, v157
	v_lshlrev_b32_e32 v58, 16, v182
	v_fmac_f32_e32 v56, v157, v157
	v_and_b32_e32 v59, 0xffff0000, v182
	v_add_f32_e32 v57, v57, v58
	v_lshlrev_b32_e32 v63, 16, v183
	v_fmac_f32_e32 v56, v58, v58
	v_add_f32_e32 v57, v57, v59
	v_and_b32_e32 v64, 0xffff0000, v183
	v_fmac_f32_e32 v56, v59, v59
	v_add_f32_e32 v57, v57, v63
	v_lshlrev_b32_e32 v65, 16, v184
	v_fmac_f32_e32 v56, v63, v63
	v_add_f32_e32 v57, v57, v64
	v_and_b32_e32 v66, 0xffff0000, v184
	v_fmac_f32_e32 v56, v64, v64
	v_add_f32_e32 v57, v57, v65
	v_lshlrev_b32_e32 v67, 16, v185
	v_fmac_f32_e32 v56, v65, v65
	v_add_f32_e32 v57, v57, v66
	v_and_b32_e32 v157, 0xffff0000, v185
	v_fmac_f32_e32 v56, v66, v66
	v_add_f32_e32 v57, v57, v67
	v_fmac_f32_e32 v56, v67, v67
	v_add_f32_e32 v57, v57, v157
	v_lshlrev_b32_e32 v58, 16, v52
	v_fmac_f32_e32 v56, v157, v157
	v_and_b32_e32 v52, 0xffff0000, v52
	v_add_f32_e32 v57, v57, v58
	v_lshlrev_b32_e32 v59, 16, v53
	v_fmac_f32_e32 v56, v58, v58
	v_add_f32_e32 v57, v57, v52
	v_and_b32_e32 v53, 0xffff0000, v53
	v_fmac_f32_e32 v56, v52, v52
	v_add_f32_e32 v52, v57, v59
	v_lshlrev_b32_e32 v63, 16, v54
	v_fmac_f32_e32 v56, v59, v59
	v_add_f32_e32 v52, v52, v53
	v_and_b32_e32 v54, 0xffff0000, v54
	v_fmac_f32_e32 v56, v53, v53
	v_add_f32_e32 v52, v52, v63
	v_lshlrev_b32_e32 v64, 16, v55
	v_fmac_f32_e32 v56, v63, v63
	v_add_f32_e32 v52, v52, v54
	v_and_b32_e32 v55, 0xffff0000, v55
	v_fmac_f32_e32 v56, v54, v54
	v_add_f32_e32 v52, v52, v64
	v_fmac_f32_e32 v56, v64, v64
	v_add_f32_e32 v52, v52, v55
	s_waitcnt vmcnt(6)
; template <int CTRL> __device__ __forceinline__ float dpp_f(float x) { return __int_as_float(__builtin_amdgcn_update_dpp(0, __float_as_int(x), CTRL, 0xF, 0xF, true)); }
; __device__ __forceinline__ void cvt8(const u32x4 r, float (&f)[8]) { f[0] = bflo(r.x); f[1] = bfhi(r.x); f[2] = bflo(r.y); f[3] = bfhi(r.y); f[4] = bflo(r.z); f[5] = bfhi(r.z); f[6] = bflo(r.w); f[7] = bfhi(r.w); }
; __device__ __forceinline__ void gmlp_unit(Ctx& C, int l, int uidx) {
;     ...
;         float s = 0.f, q = 0.f;
; #pragma unroll
;         for (int c8 = 0; c8 < 16; ++c8) { float f[8]; cvt8(r1[c8], f);
; #pragma unroll
;             for (int j = 0; j < 8; ++j) { s += f[j]; q += f[j] * f[j]; } }
;         s += dpp_f<DPP_XOR1>(s); s += dpp_f<DPP_XOR2>(s); q += dpp_f<DPP_XOR1>(q); q += dpp_f<DPP_XOR2>(q);
;         const float mean = s * (1.0f / 512.0f); const float var = fmaxf(q * (1.0f / 512.0f) - mean * mean, 0.f); const float rstd = 1.0f / sqrtf(var + LN_EPS);
;         const float* lg = INP(I_GLG) + l * 512 + 256 * hf + 64 * part; const float* lb = INP(I_GLB) + l * 512 + 256 * hf + 64 * part;
; #pragma unroll
;         for (int c8 = 0; c8 < 8; ++c8) { float f[8]; cvt8(r2[c8], f);
;             const f32x4 g0 = *(const f32x4*)(lg + 8 * c8), g1 = *(const f32x4*)(lg + 8 * c8 + 4), b0 = *(const f32x4*)(lb + 8 * c8), b1 = *(const f32x4*)(lb + 8 * c8 + 4);
	v_lshlrev_b32_e32 v53, 16, v48
	v_fmac_f32_e32 v56, v55, v55
	v_and_b32_e32 v48, 0xffff0000, v48
	v_add_f32_e32 v52, v52, v53
	v_lshlrev_b32_e32 v54, 16, v49
	v_fmac_f32_e32 v56, v53, v53
	v_add_f32_e32 v52, v52, v48
	v_and_b32_e32 v49, 0xffff0000, v49
	v_fmac_f32_e32 v56, v48, v48
	v_add_f32_e32 v48, v52, v54
	v_lshlrev_b32_e32 v55, 16, v50
	v_fmac_f32_e32 v56, v54, v54
	v_add_f32_e32 v48, v48, v49
	v_and_b32_e32 v50, 0xffff0000, v50
	v_fmac_f32_e32 v56, v49, v49
	v_add_f32_e32 v48, v48, v55
	v_lshlrev_b32_e32 v57, 16, v51
	v_fmac_f32_e32 v56, v55, v55
	v_add_f32_e32 v48, v48, v50
	v_and_b32_e32 v51, 0xffff0000, v51
	v_fmac_f32_e32 v56, v50, v50
	v_add_f32_e32 v48, v48, v57
	v_fmac_f32_e32 v56, v57, v57
	v_add_f32_e32 v48, v48, v51
	v_lshlrev_b32_e32 v49, 16, v44
	v_fmac_f32_e32 v56, v51, v51
	v_and_b32_e32 v44, 0xffff0000, v44
	v_add_f32_e32 v48, v48, v49
	v_lshlrev_b32_e32 v50, 16, v45
	v_fmac_f32_e32 v56, v49, v49
	v_add_f32_e32 v48, v48, v44
	v_and_b32_e32 v45, 0xffff0000, v45
	v_fmac_f32_e32 v56, v44, v44
	v_add_f32_e32 v44, v48, v50
	v_lshlrev_b32_e32 v51, 16, v46
	v_fmac_f32_e32 v56, v50, v50
	v_add_f32_e32 v44, v44, v45
	v_and_b32_e32 v46, 0xffff0000, v46
	v_fmac_f32_e32 v56, v45, v45
	v_add_f32_e32 v44, v44, v51
	v_lshlrev_b32_e32 v52, 16, v47
	v_fmac_f32_e32 v56, v51, v51
	v_add_f32_e32 v44, v44, v46
	v_and_b32_e32 v47, 0xffff0000, v47
	v_fmac_f32_e32 v56, v46, v46
	v_add_f32_e32 v44, v44, v52
	v_fmac_f32_e32 v56, v52, v52
	v_add_f32_e32 v44, v44, v47
	v_lshlrev_b32_e32 v45, 16, v40
	v_fmac_f32_e32 v56, v47, v47
	v_and_b32_e32 v40, 0xffff0000, v40
	v_add_f32_e32 v44, v44, v45
	v_lshlrev_b32_e32 v46, 16, v41
	v_fmac_f32_e32 v56, v45, v45
	v_add_f32_e32 v44, v44, v40
	v_and_b32_e32 v41, 0xffff0000, v41
	v_fmac_f32_e32 v56, v40, v40
	v_add_f32_e32 v40, v44, v46
	v_lshlrev_b32_e32 v47, 16, v42
	v_fmac_f32_e32 v56, v46, v46
	v_add_f32_e32 v40, v40, v41
	v_and_b32_e32 v42, 0xffff0000, v42
	v_fmac_f32_e32 v56, v41, v41
	v_add_f32_e32 v40, v40, v47
	v_lshlrev_b32_e32 v48, 16, v43
	v_fmac_f32_e32 v56, v47, v47
	v_add_f32_e32 v40, v40, v42
	v_and_b32_e32 v43, 0xffff0000, v43
	v_fmac_f32_e32 v56, v42, v42
	v_add_f32_e32 v40, v40, v48
	v_fmac_f32_e32 v56, v48, v48
	v_add_f32_e32 v40, v40, v43
	v_lshlrev_b32_e32 v41, 16, v36
	v_fmac_f32_e32 v56, v43, v43
	v_and_b32_e32 v36, 0xffff0000, v36
	v_add_f32_e32 v40, v40, v41
	v_lshlrev_b32_e32 v42, 16, v37
	v_fmac_f32_e32 v56, v41, v41
	v_add_f32_e32 v40, v40, v36
	v_and_b32_e32 v37, 0xffff0000, v37
	v_fmac_f32_e32 v56, v36, v36
	v_add_f32_e32 v36, v40, v42
	v_lshlrev_b32_e32 v43, 16, v38
	v_fmac_f32_e32 v56, v42, v42
	v_add_f32_e32 v36, v36, v37
	v_and_b32_e32 v38, 0xffff0000, v38
	v_fmac_f32_e32 v56, v37, v37
	v_add_f32_e32 v36, v36, v43
	v_lshlrev_b32_e32 v44, 16, v39
	v_fmac_f32_e32 v56, v43, v43
	v_add_f32_e32 v36, v36, v38
	v_and_b32_e32 v39, 0xffff0000, v39
	v_fmac_f32_e32 v56, v38, v38
	v_add_f32_e32 v36, v36, v44
	v_fmac_f32_e32 v56, v44, v44
	v_add_f32_e32 v36, v36, v39
	s_waitcnt vmcnt(2)
	v_lshlrev_b32_e32 v37, 16, v32
	v_fmac_f32_e32 v56, v39, v39
	v_and_b32_e32 v32, 0xffff0000, v32
	v_add_f32_e32 v36, v36, v37
	v_lshlrev_b32_e32 v38, 16, v33
	v_fmac_f32_e32 v56, v37, v37
	v_add_f32_e32 v36, v36, v32
	v_and_b32_e32 v33, 0xffff0000, v33
	v_fmac_f32_e32 v56, v32, v32
	v_add_f32_e32 v32, v36, v38
	v_lshlrev_b32_e32 v39, 16, v34
	v_fmac_f32_e32 v56, v38, v38
	v_add_f32_e32 v32, v32, v33
	v_and_b32_e32 v34, 0xffff0000, v34
	v_fmac_f32_e32 v56, v33, v33
	v_add_f32_e32 v32, v32, v39
	v_lshlrev_b32_e32 v40, 16, v35
	v_fmac_f32_e32 v56, v39, v39
	v_add_f32_e32 v32, v32, v34
	v_and_b32_e32 v35, 0xffff0000, v35
	v_fmac_f32_e32 v56, v34, v34
	v_add_f32_e32 v32, v32, v40
	v_fmac_f32_e32 v56, v40, v40
	v_add_f32_e32 v32, v32, v35
	v_lshlrev_b32_e32 v33, 16, v24
	v_fmac_f32_e32 v56, v35, v35
	v_and_b32_e32 v24, 0xffff0000, v24
	v_add_f32_e32 v32, v32, v33
	v_lshlrev_b32_e32 v34, 16, v25
	v_fmac_f32_e32 v56, v33, v33
	v_add_f32_e32 v32, v32, v24
	v_and_b32_e32 v25, 0xffff0000, v25
	v_fmac_f32_e32 v56, v24, v24
	v_add_f32_e32 v24, v32, v34
	v_lshlrev_b32_e32 v35, 16, v26
	v_fmac_f32_e32 v56, v34, v34
	v_add_f32_e32 v24, v24, v25
	v_and_b32_e32 v26, 0xffff0000, v26
	v_fmac_f32_e32 v56, v25, v25
	v_add_f32_e32 v24, v24, v35
	v_lshlrev_b32_e32 v36, 16, v27
	v_fmac_f32_e32 v56, v35, v35
	v_add_f32_e32 v24, v24, v26
	v_and_b32_e32 v27, 0xffff0000, v27
	v_fmac_f32_e32 v56, v26, v26
	v_add_f32_e32 v24, v24, v36
	v_fmac_f32_e32 v56, v36, v36
	v_add_f32_e32 v24, v24, v27
	v_lshlrev_b32_e32 v25, 16, v20
	v_fmac_f32_e32 v56, v27, v27
	v_and_b32_e32 v20, 0xffff0000, v20
	v_add_f32_e32 v24, v24, v25
	v_lshlrev_b32_e32 v26, 16, v21
	v_fmac_f32_e32 v56, v25, v25
	v_add_f32_e32 v24, v24, v20
	v_and_b32_e32 v21, 0xffff0000, v21
	v_fmac_f32_e32 v56, v20, v20
	v_add_f32_e32 v20, v24, v26
	v_lshlrev_b32_e32 v27, 16, v22
	v_fmac_f32_e32 v56, v26, v26
	v_add_f32_e32 v20, v20, v21
	v_and_b32_e32 v22, 0xffff0000, v22
	v_fmac_f32_e32 v56, v21, v21
	v_add_f32_e32 v20, v20, v27
	v_lshlrev_b32_e32 v32, 16, v23
	v_fmac_f32_e32 v56, v27, v27
	v_add_f32_e32 v20, v20, v22
	v_and_b32_e32 v23, 0xffff0000, v23
	v_fmac_f32_e32 v56, v22, v22
	v_add_f32_e32 v20, v20, v32
	v_fmac_f32_e32 v56, v32, v32
	v_add_f32_e32 v20, v20, v23
	v_lshlrev_b32_e32 v21, 16, v12
	v_fmac_f32_e32 v56, v23, v23
	v_and_b32_e32 v12, 0xffff0000, v12
	v_add_f32_e32 v20, v20, v21
	v_lshlrev_b32_e32 v22, 16, v13
	v_fmac_f32_e32 v56, v21, v21
	v_add_f32_e32 v20, v20, v12
	v_and_b32_e32 v13, 0xffff0000, v13
	v_fmac_f32_e32 v56, v12, v12
	v_add_f32_e32 v12, v20, v22
	v_lshlrev_b32_e32 v23, 16, v14
	v_add_f32_e32 v12, v12, v13
	v_and_b32_e32 v14, 0xffff0000, v14
	v_fmac_f32_e32 v56, v22, v22
	v_add_f32_e32 v12, v12, v23
	v_lshlrev_b32_e32 v24, 16, v15
	v_fmac_f32_e32 v56, v13, v13
	v_add_f32_e32 v12, v12, v14
	v_and_b32_e32 v15, 0xffff0000, v15
	v_fmac_f32_e32 v56, v23, v23
	v_add_f32_e32 v12, v12, v24
	v_fmac_f32_e32 v56, v14, v14
	v_add_f32_e32 v12, v12, v15
	global_load_dwordx4 v[174:177], v158, s[8:9] offset:2048
	global_load_dwordx4 v[178:181], v158, s[10:11] offset:2048
	v_fmac_f32_e32 v56, v24, v24
	v_add_f32_dpp v12, v12, v12 quad_perm:[1,0,3,2] row_mask:0xf bank_mask:0xf bound_ctrl:1
	v_fmac_f32_e32 v56, v15, v15
	global_load_dwordx4 v[44:47], v158, s[8:9] offset:2064
	global_load_dwordx4 v[48:51], v158, s[10:11] offset:2064
	v_add_f32_dpp v157, v12, v12 quad_perm:[2,3,0,1] row_mask:0xf bank_mask:0xf bound_ctrl:1
	v_add_f32_dpp v12, v56, v56 quad_perm:[1,0,3,2] row_mask:0xf bank_mask:0xf bound_ctrl:1
	v_mul_f32_e32 v13, 0x3b000000, v157
	v_mul_f32_e32 v13, v13, v13
	v_add_f32_dpp v12, v12, v12 quad_perm:[2,3,0,1] row_mask:0xf bank_mask:0xf bound_ctrl:1
	v_fma_f32 v12, v12, s6, -v13
	v_max_f32_e32 v12, 0, v12
	v_add_f32_e32 v12, 0x358637bd, v12
	s_mov_b32 s6, 0xf800000
	v_mul_f32_e32 v13, 0x4f800000, v12
	v_cmp_gt_f32_e32 vcc, s6, v12
	v_lshlrev_b32_e32 v164, 1, v62
	s_waitcnt vmcnt(4)
; #define LAS __attribute__((address_space(3)))
; __device__ __forceinline__ unsigned pk2(float lo, float hi) { f32x2 v = {lo, hi}; bf16x2_t b = __builtin_convertvector(v, bf16x2_t); return __builtin_bit_cast(unsigned, b); }
; __device__ __forceinline__ void cvt8(const u32x4 r, float (&f)[8]) { f[0] = bflo(r.x); f[1] = bfhi(r.x); f[2] = bflo(r.y); f[3] = bfhi(r.y); f[4] = bflo(r.z); f[5] = bfhi(r.z); f[6] = bflo(r.w); f[7] = bfhi(r.w); }
; __device__ __forceinline__ void gmlp_unit(Ctx& C, int l, int uidx) {
;     ...
;         const float mean = s * (1.0f / 512.0f); const float var = fmaxf(q * (1.0f / 512.0f) - mean * mean, 0.f); const float rstd = 1.0f / sqrtf(var + LN_EPS);
;         const float* lg = INP(I_GLG) + l * 512 + 256 * hf + 64 * part; const float* lb = INP(I_GLB) + l * 512 + 256 * hf + 64 * part;
; #pragma unroll
;         for (int c8 = 0; c8 < 8; ++c8) { float f[8]; cvt8(r2[c8], f);
;             const f32x4 g0 = *(const f32x4*)(lg + 8 * c8), g1 = *(const f32x4*)(lg + 8 * c8 + 4), b0 = *(const f32x4*)(lb + 8 * c8), b1 = *(const f32x4*)(lb + 8 * c8 + 4);
;             const float gg[8] = {g0[0], g0[1], g0[2], g0[3], g1[0], g1[1], g1[2], g1[3]}, bb[8] = {b0[0], b0[1], b0[2], b0[3], b1[0], b1[1], b1[2], b1[3]};
; #pragma unroll
;             for (int j = 0; j < 8; ++j) { const float vn = (f[j] - mean) * rstd * gg[j] + bb[j];
;                 *(LAS bf16*)(C.lds + (64 * part + 8 * c8 + j) * VS + tok * 2) = (bf16)(pk2(vn, 0.f) & 0xffffu); } }
	v_lshlrev_b32_e32 v173, 16, v28
	v_cndmask_b32_e32 v24, v12, v13, vcc
	v_sqrt_f32_e32 v25, v24
	global_load_dwordx4 v[36:39], v[60:61], off offset:48
	global_load_dwordx4 v[40:43], v[60:61], off offset:32
	global_load_dwordx4 v[12:15], v[60:61], off offset:112
	global_load_dwordx4 v[20:23], v[60:61], off offset:96
	v_and_b32_e32 v28, 0xffff0000, v28
	v_fmac_f32_e32 v28, 0xbb000000, v157
	v_add_u32_e32 v26, -1, v25
	v_fma_f32 v27, -v26, v25, v24
	v_cmp_ge_f32_e64 s[6:7], 0, v27
	v_add_u32_e32 v27, 1, v25
	v_lshlrev_b32_e32 v182, 16, v29
	v_cndmask_b32_e64 v26, v25, v26, s[6:7]
	v_fma_f32 v25, -v27, v25, v24
	v_cmp_lt_f32_e64 s[6:7], 0, v25
	v_add3_u32 v162, 0, v164, v162
	v_fmac_f32_e32 v182, 0xbb000000, v157
	v_cndmask_b32_e64 v25, v26, v27, s[6:7]
	v_mul_f32_e32 v26, 0x37800000, v25
	v_cndmask_b32_e32 v25, v25, v26, vcc
	v_cmp_class_f32_e32 vcc, v24, v163
	v_and_b32_e32 v29, 0xffff0000, v29
	v_fmac_f32_e32 v29, 0xbb000000, v157
	v_cndmask_b32_e32 v63, v25, v24, vcc
	v_div_scale_f32 v64, s[6:7], v63, v63, 1.0
	v_rcp_f32_e32 v65, v64
	global_load_dwordx4 v[52:55], v158, s[8:9] offset:2080
	global_load_dwordx4 v[56:59], v158, s[10:11] offset:2080
	global_load_dwordx4 v[24:27], v[60:61], off offset:80
	global_load_dwordx4 v[32:35], v[60:61], off offset:64
	v_lshlrev_b32_e32 v183, 16, v30
	v_fmac_f32_e32 v173, 0xbb000000, v157
	v_fma_f32 v60, -v64, v65, 1.0
	v_fmac_f32_e32 v65, v60, v65
	v_div_scale_f32 v60, vcc, 1.0, v63, 1.0
	v_mul_f32_e32 v61, v60, v65
	v_fma_f32 v66, -v64, v61, v60
	v_fmac_f32_e32 v61, v66, v65
	v_fma_f32 v60, -v64, v61, v60
	v_div_fmas_f32 v60, v60, v65, v61
	v_div_fixup_f32 v159, v60, v63, 1.0
	global_load_dwordx4 v[60:63], v158, s[8:9] offset:2096
	global_load_dwordx4 v[64:67], v158, s[10:11] offset:2096
	v_mul_f32_e32 v28, v28, v159
	v_fmac_f32_e32 v183, 0xbb000000, v157
	v_mul_f32_e32 v173, v173, v159
	v_and_b32_e32 v30, 0xffff0000, v30
	v_fmac_f32_e32 v30, 0xbb000000, v157
	v_lshlrev_b32_e32 v184, 16, v31
	v_fmac_f32_e32 v184, 0xbb000000, v157
	v_and_b32_e32 v31, 0xffff0000, v31
	v_fmac_f32_e32 v31, 0xbb000000, v157
	s_movk_i32 s6, 0x110
	s_waitcnt vmcnt(12)
	v_fma_f32 v28, v175, v28, v179
	v_cvt_pk_bf16_f32 v28, v28, s0
	ds_write_b16 v162, v28 offset:272
	v_mul_f32_e32 v28, v182, v159
	v_fma_f32 v28, v176, v28, v180
	v_cvt_pk_bf16_f32 v28, v28, s0
	ds_write_b16 v162, v28 offset:544
	v_mul_f32_e32 v28, v29, v159
	v_fmac_f32_e32 v181, v177, v28
	v_cvt_pk_bf16_f32 v28, v181, s0
	ds_write_b16 v162, v28 offset:816
	v_mul_f32_e32 v28, v183, v159
	v_fma_f32 v173, v174, v173, v178
	s_waitcnt vmcnt(10)
	v_fma_f32 v28, v44, v28, v48
	v_cvt_pk_bf16_f32 v173, v173, s0
	v_cvt_pk_bf16_f32 v28, v28, s0
	ds_write_b16 v162, v173
	ds_write_b16 v162, v28 offset:1088
	v_mul_f32_e32 v28, v30, v159
	global_load_dwordx4 v[174:177], v158, s[8:9] offset:2112
	global_load_dwordx4 v[178:181], v158, s[10:11] offset:2112
	v_fma_f32 v28, v45, v28, v49
	v_cvt_pk_bf16_f32 v28, v28, s0
	ds_write_b16 v162, v28 offset:1360
	v_mul_f32_e32 v28, v184, v159
	v_fma_f32 v28, v46, v28, v50
	v_cvt_pk_bf16_f32 v28, v28, s0
	ds_write_b16 v162, v28 offset:1632
	v_mul_f32_e32 v28, v31, v159
	v_fmac_f32_e32 v51, v47, v28
	v_cvt_pk_bf16_f32 v28, v51, s0
	ds_write_b16 v162, v28 offset:1904
	global_load_dwordx4 v[28:31], v158, s[8:9] offset:2128
	global_load_dwordx4 v[48:51], v158, s[10:11] offset:2128
	v_lshlrev_b32_e32 v44, 16, v16
	v_and_b32_e32 v16, 0xffff0000, v16
	v_fmac_f32_e32 v16, 0xbb000000, v157
	v_mul_f32_e32 v16, v16, v159
	v_lshlrev_b32_e32 v45, 16, v17
	v_fmac_f32_e32 v45, 0xbb000000, v157
	v_and_b32_e32 v17, 0xffff0000, v17
	v_fmac_f32_e32 v17, 0xbb000000, v157
	v_lshlrev_b32_e32 v46, 16, v18
	s_waitcnt vmcnt(8)
	v_fma_f32 v16, v53, v16, v57
	v_cvt_pk_bf16_f32 v16, v16, s0
	ds_write_b16 v162, v16 offset:2448
	v_mul_f32_e32 v16, v45, v159
	v_fma_f32 v16, v54, v16, v58
	v_cvt_pk_bf16_f32 v16, v16, s0
	ds_write_b16 v162, v16 offset:2720
	v_mul_f32_e32 v16, v17, v159
	v_fmac_f32_e32 v59, v55, v16
	v_fmac_f32_e32 v44, 0xbb000000, v157
	v_cvt_pk_bf16_f32 v16, v59, s0
	v_fmac_f32_e32 v46, 0xbb000000, v157
	v_mul_f32_e32 v44, v44, v159
	ds_write_b16 v162, v16 offset:2992
	v_mul_f32_e32 v16, v46, v159
	v_and_b32_e32 v18, 0xffff0000, v18
	v_fma_f32 v44, v52, v44, v56
	s_waitcnt vmcnt(4)
	v_fma_f32 v16, v60, v16, v64
	v_cvt_pk_bf16_f32 v44, v44, s0
	v_cvt_pk_bf16_f32 v16, v16, s0
	v_fmac_f32_e32 v18, 0xbb000000, v157
	ds_write_b16 v162, v44 offset:2176
	ds_write_b16 v162, v16 offset:3264
	v_mul_f32_e32 v16, v18, v159
	v_lshlrev_b32_e32 v47, 16, v19
	global_load_dwordx4 v[52:55], v158, s[8:9] offset:2144
	global_load_dwordx4 v[56:59], v158, s[10:11] offset:2144
	v_fma_f32 v16, v61, v16, v65
	v_cvt_pk_bf16_f32 v16, v16, s0
	v_fmac_f32_e32 v47, 0xbb000000, v157
	ds_write_b16 v162, v16 offset:3536
	v_mul_f32_e32 v16, v47, v159
	v_and_b32_e32 v19, 0xffff0000, v19
	v_fma_f32 v16, v62, v16, v66
	v_cvt_pk_bf16_f32 v16, v16, s0
	v_fmac_f32_e32 v19, 0xbb000000, v157
	ds_write_b16 v162, v16 offset:3808
	v_mul_f32_e32 v16, v19, v159
	v_fmac_f32_e32 v67, v63, v16
	v_cvt_pk_bf16_f32 v16, v67, s0
	ds_write_b16 v162, v16 offset:4080
	global_load_dwordx4 v[16:19], v158, s[8:9] offset:2160
	global_load_dwordx4 v[44:47], v158, s[10:11] offset:2160
	v_lshlrev_b32_e32 v60, 16, v40
	v_and_b32_e32 v40, 0xffff0000, v40
	v_fmac_f32_e32 v40, 0xbb000000, v157
	v_mul_f32_e32 v40, v40, v159
	v_lshlrev_b32_e32 v61, 16, v41
	v_fmac_f32_e32 v61, 0xbb000000, v157
	v_and_b32_e32 v41, 0xffff0000, v41
	v_fmac_f32_e32 v41, 0xbb000000, v157
	v_lshlrev_b32_e32 v62, 16, v42
	v_fmac_f32_e32 v60, 0xbb000000, v157
	v_fmac_f32_e32 v62, 0xbb000000, v157
	v_mul_f32_e32 v60, v60, v159
	v_and_b32_e32 v42, 0xffff0000, v42
	v_fmac_f32_e32 v42, 0xbb000000, v157
	v_lshlrev_b32_e32 v164, 16, v43
	v_fmac_f32_e32 v164, 0xbb000000, v157
	v_and_b32_e32 v43, 0xffff0000, v43
	s_waitcnt vmcnt(6)
; #define LAS __attribute__((address_space(3)))
; __device__ __forceinline__ unsigned pk2(float lo, float hi) { f32x2 v = {lo, hi}; bf16x2_t b = __builtin_convertvector(v, bf16x2_t); return __builtin_bit_cast(unsigned, b); }
; __device__ __forceinline__ void cvt8(const u32x4 r, float (&f)[8]) { f[0] = bflo(r.x); f[1] = bfhi(r.x); f[2] = bflo(r.y); f[3] = bfhi(r.y); f[4] = bflo(r.z); f[5] = bfhi(r.z); f[6] = bflo(r.w); f[7] = bfhi(r.w); }
; __device__ __forceinline__ void gmlp_unit(Ctx& C, int l, int uidx) {
;     ...
;         for (int c8 = 0; c8 < 8; ++c8) { float f[8]; cvt8(r2[c8], f);
;             const f32x4 g0 = *(const f32x4*)(lg + 8 * c8), g1 = *(const f32x4*)(lg + 8 * c8 + 4), b0 = *(const f32x4*)(lb + 8 * c8), b1 = *(const f32x4*)(lb + 8 * c8 + 4);
;             const float gg[8] = {g0[0], g0[1], g0[2], g0[3], g1[0], g1[1], g1[2], g1[3]}, bb[8] = {b0[0], b0[1], b0[2], b0[3], b1[0], b1[1], b1[2], b1[3]};
; #pragma unroll
;             for (int j = 0; j < 8; ++j) { const float vn = (f[j] - mean) * rstd * gg[j] + bb[j];
;                 *(LAS bf16*)(C.lds + (64 * part + 8 * c8 + j) * VS + tok * 2) = (bf16)(pk2(vn, 0.f) & 0xffffu); } }
	v_fma_f32 v40, v175, v40, v179
	v_cvt_pk_bf16_f32 v40, v40, s0
	ds_write_b16 v162, v40 offset:4624
	v_mul_f32_e32 v40, v61, v159
	v_fma_f32 v40, v176, v40, v180
	v_cvt_pk_bf16_f32 v40, v40, s0
	ds_write_b16 v162, v40 offset:4896
	v_mul_f32_e32 v40, v41, v159
	v_fmac_f32_e32 v181, v177, v40
	v_cvt_pk_bf16_f32 v40, v181, s0
	ds_write_b16 v162, v40 offset:5168
	v_mul_f32_e32 v40, v62, v159
	v_fma_f32 v60, v174, v60, v178
	s_waitcnt vmcnt(4)
	v_fma_f32 v28, v28, v40, v48
	v_cvt_pk_bf16_f32 v60, v60, s0
	v_cvt_pk_bf16_f32 v28, v28, s0
	ds_write_b16 v162, v60 offset:4352
	ds_write_b16 v162, v28 offset:5440
	v_mul_f32_e32 v28, v42, v159
	global_load_dwordx4 v[60:63], v158, s[8:9] offset:2176
	global_load_dwordx4 v[64:67], v158, s[10:11] offset:2176
	v_fma_f32 v28, v29, v28, v49
	v_cvt_pk_bf16_f32 v28, v28, s0
	ds_write_b16 v162, v28 offset:5712
	v_mul_f32_e32 v28, v164, v159
	v_fma_f32 v28, v30, v28, v50
	v_cvt_pk_bf16_f32 v28, v28, s0
	v_fmac_f32_e32 v43, 0xbb000000, v157
	ds_write_b16 v162, v28 offset:5984
	v_mul_f32_e32 v28, v43, v159
	v_fmac_f32_e32 v51, v31, v28
	v_cvt_pk_bf16_f32 v28, v51, s0
	ds_write_b16 v162, v28 offset:6256
	global_load_dwordx4 v[28:31], v158, s[8:9] offset:2192
	global_load_dwordx4 v[40:43], v158, s[10:11] offset:2192
	v_lshlrev_b32_e32 v48, 16, v36
	v_and_b32_e32 v36, 0xffff0000, v36
	v_fmac_f32_e32 v36, 0xbb000000, v157
	v_mul_f32_e32 v36, v36, v159
	v_lshlrev_b32_e32 v49, 16, v37
	v_fmac_f32_e32 v49, 0xbb000000, v157
	v_and_b32_e32 v37, 0xffff0000, v37
	v_fmac_f32_e32 v37, 0xbb000000, v157
	v_lshlrev_b32_e32 v50, 16, v38
	v_fmac_f32_e32 v50, 0xbb000000, v157
	v_fmac_f32_e32 v48, 0xbb000000, v157
	v_and_b32_e32 v164, 0xffff0000, v38
	v_mul_f32_e32 v38, v48, v159
	v_fmac_f32_e32 v164, 0xbb000000, v157
	s_waitcnt vmcnt(6)
	v_fma_f32 v36, v53, v36, v57
	v_cvt_pk_bf16_f32 v36, v36, s0
	ds_write_b16 v162, v36 offset:6800
	v_mul_f32_e32 v36, v49, v159
	v_fma_f32 v36, v54, v36, v58
	v_cvt_pk_bf16_f32 v36, v36, s0
	ds_write_b16 v162, v36 offset:7072
	v_mul_f32_e32 v36, v37, v159
	v_fmac_f32_e32 v59, v55, v36
	v_cvt_pk_bf16_f32 v36, v59, s0
	ds_write_b16 v162, v36 offset:7344
	v_mul_f32_e32 v36, v50, v159
	v_fma_f32 v38, v52, v38, v56
	v_cvt_pk_bf16_f32 v38, v38, s0
	v_lshlrev_b32_e32 v173, 16, v39
	s_waitcnt vmcnt(4)
	v_fma_f32 v16, v16, v36, v44
	v_cvt_pk_bf16_f32 v16, v16, s0
	ds_write_b16 v162, v16 offset:7616
	v_mul_f32_e32 v16, v164, v159
	ds_write_b16 v162, v38 offset:6528
	v_fma_f32 v16, v17, v16, v45
	v_and_b32_e32 v174, 0xffff0000, v39
	global_load_dwordx4 v[36:39], v158, s[8:9] offset:2208
	global_load_dwordx4 v[48:51], v158, s[10:11] offset:2208
	v_cvt_pk_bf16_f32 v16, v16, s0
	v_fmac_f32_e32 v173, 0xbb000000, v157
	ds_write_b16 v162, v16 offset:7888
	v_mul_f32_e32 v16, v173, v159
	v_fma_f32 v16, v18, v16, v46
	v_cvt_pk_bf16_f32 v16, v16, s0
	v_fmac_f32_e32 v174, 0xbb000000, v157
	ds_write_b16 v162, v16 offset:8160
	v_mul_f32_e32 v16, v174, v159
	v_fmac_f32_e32 v47, v19, v16
	v_cvt_pk_bf16_f32 v16, v47, s0
	ds_write_b16 v162, v16 offset:8432
	global_load_dwordx4 v[16:19], v158, s[8:9] offset:2224
	global_load_dwordx4 v[44:47], v158, s[10:11] offset:2224
	v_lshlrev_b32_e32 v52, 16, v32
	v_and_b32_e32 v32, 0xffff0000, v32
	v_fmac_f32_e32 v32, 0xbb000000, v157
	v_mul_f32_e32 v32, v32, v159
	v_lshlrev_b32_e32 v53, 16, v33
	v_fmac_f32_e32 v53, 0xbb000000, v157
	v_and_b32_e32 v33, 0xffff0000, v33
	v_fmac_f32_e32 v33, 0xbb000000, v157
	v_lshlrev_b32_e32 v54, 16, v34
	v_fmac_f32_e32 v52, 0xbb000000, v157
	v_fmac_f32_e32 v54, 0xbb000000, v157
	v_and_b32_e32 v56, 0xffff0000, v34
	v_mul_f32_e32 v34, v52, v159
	v_fmac_f32_e32 v56, 0xbb000000, v157
	v_lshlrev_b32_e32 v57, 16, v35
	v_and_b32_e32 v58, 0xffff0000, v35
	s_waitcnt vmcnt(6)
	v_fma_f32 v32, v61, v32, v65
	v_cvt_pk_bf16_f32 v32, v32, s0
	ds_write_b16 v162, v32 offset:8976
	v_mul_f32_e32 v32, v53, v159
	v_fma_f32 v32, v62, v32, v66
	v_cvt_pk_bf16_f32 v32, v32, s0
	ds_write_b16 v162, v32 offset:9248
	v_mul_f32_e32 v32, v33, v159
	v_fmac_f32_e32 v67, v63, v32
	v_cvt_pk_bf16_f32 v32, v67, s0
	ds_write_b16 v162, v32 offset:9520
	v_mul_f32_e32 v32, v54, v159
	v_fma_f32 v34, v60, v34, v64
	s_waitcnt vmcnt(4)
	v_fma_f32 v28, v28, v32, v40
	v_cvt_pk_bf16_f32 v34, v34, s0
	v_cvt_pk_bf16_f32 v28, v28, s0
	ds_write_b16 v162, v34 offset:8704
	ds_write_b16 v162, v28 offset:9792
	v_mul_f32_e32 v28, v56, v159
	global_load_dwordx4 v[32:35], v158, s[8:9] offset:2240
	global_load_dwordx4 v[52:55], v158, s[10:11] offset:2240
	v_fma_f32 v28, v29, v28, v41
	v_cvt_pk_bf16_f32 v28, v28, s0
	v_fmac_f32_e32 v57, 0xbb000000, v157
	ds_write_b16 v162, v28 offset:10064
	v_mul_f32_e32 v28, v57, v159
	v_fma_f32 v28, v30, v28, v42
	v_cvt_pk_bf16_f32 v28, v28, s0
	v_fmac_f32_e32 v58, 0xbb000000, v157
	ds_write_b16 v162, v28 offset:10336
	v_mul_f32_e32 v28, v58, v159
	v_fmac_f32_e32 v43, v31, v28
	v_cvt_pk_bf16_f32 v28, v43, s0
	ds_write_b16 v162, v28 offset:10608
	global_load_dwordx4 v[28:31], v158, s[8:9] offset:2256
	global_load_dwordx4 v[40:43], v158, s[10:11] offset:2256
	v_lshlrev_b32_e32 v56, 16, v24
	v_and_b32_e32 v24, 0xffff0000, v24
	v_fmac_f32_e32 v24, 0xbb000000, v157
	v_mul_f32_e32 v24, v24, v159
	v_lshlrev_b32_e32 v57, 16, v25
	v_fmac_f32_e32 v57, 0xbb000000, v157
	v_and_b32_e32 v25, 0xffff0000, v25
	v_fmac_f32_e32 v56, 0xbb000000, v157
	v_fmac_f32_e32 v25, 0xbb000000, v157
	v_lshlrev_b32_e32 v58, 16, v26
	v_and_b32_e32 v59, 0xffff0000, v26
	v_mul_f32_e32 v26, v56, v159
	v_fmac_f32_e32 v58, 0xbb000000, v157
	v_lshlrev_b32_e32 v60, 16, v27
	v_and_b32_e32 v61, 0xffff0000, v27
	v_fmac_f32_e32 v59, 0xbb000000, v157
	s_waitcnt vmcnt(6)
; #define LAS __attribute__((address_space(3)))
; __device__ __forceinline__ unsigned pk2(float lo, float hi) { f32x2 v = {lo, hi}; bf16x2_t b = __builtin_convertvector(v, bf16x2_t); return __builtin_bit_cast(unsigned, b); }
; __device__ __forceinline__ void cvt8(const u32x4 r, float (&f)[8]) { f[0] = bflo(r.x); f[1] = bfhi(r.x); f[2] = bflo(r.y); f[3] = bfhi(r.y); f[4] = bflo(r.z); f[5] = bfhi(r.z); f[6] = bflo(r.w); f[7] = bfhi(r.w); }
; __device__ __forceinline__ void gmlp_unit(Ctx& C, int l, int uidx) {
;     ...
;         for (int c8 = 0; c8 < 8; ++c8) { float f[8]; cvt8(r2[c8], f);
;             const f32x4 g0 = *(const f32x4*)(lg + 8 * c8), g1 = *(const f32x4*)(lg + 8 * c8 + 4), b0 = *(const f32x4*)(lb + 8 * c8), b1 = *(const f32x4*)(lb + 8 * c8 + 4);
;             const float gg[8] = {g0[0], g0[1], g0[2], g0[3], g1[0], g1[1], g1[2], g1[3]}, bb[8] = {b0[0], b0[1], b0[2], b0[3], b1[0], b1[1], b1[2], b1[3]};
; #pragma unroll
;             for (int j = 0; j < 8; ++j) { const float vn = (f[j] - mean) * rstd * gg[j] + bb[j];
;                 *(LAS bf16*)(C.lds + (64 * part + 8 * c8 + j) * VS + tok * 2) = (bf16)(pk2(vn, 0.f) & 0xffffu); } }
;     }
;     __syncthreads();
	v_fma_f32 v24, v37, v24, v49
	v_cvt_pk_bf16_f32 v24, v24, s0
	ds_write_b16 v162, v24 offset:11152
	v_mul_f32_e32 v24, v57, v159
	v_fma_f32 v24, v38, v24, v50
	v_cvt_pk_bf16_f32 v24, v24, s0
	ds_write_b16 v162, v24 offset:11424
	v_mul_f32_e32 v24, v25, v159
	v_fma_f32 v26, v36, v26, v48
	v_fmac_f32_e32 v51, v39, v24
	v_cvt_pk_bf16_f32 v26, v26, s0
	v_cvt_pk_bf16_f32 v24, v51, s0
	v_mul_f32_e32 v48, v58, v159
	ds_write_b16 v162, v26 offset:10880
	ds_write_b16 v162, v24 offset:11696
	s_waitcnt vmcnt(4)
	v_fma_f32 v16, v16, v48, v44
	global_load_dwordx4 v[24:27], v158, s[8:9] offset:2272
	global_load_dwordx4 v[36:39], v158, s[10:11] offset:2272
	v_cvt_pk_bf16_f32 v16, v16, s0
	ds_write_b16 v162, v16 offset:11968
	v_mul_f32_e32 v16, v59, v159
	v_fma_f32 v16, v17, v16, v45
	v_cvt_pk_bf16_f32 v16, v16, s0
	v_fmac_f32_e32 v60, 0xbb000000, v157
	ds_write_b16 v162, v16 offset:12240
	v_mul_f32_e32 v16, v60, v159
	v_fma_f32 v16, v18, v16, v46
	v_cvt_pk_bf16_f32 v16, v16, s0
	v_fmac_f32_e32 v61, 0xbb000000, v157
	ds_write_b16 v162, v16 offset:12512
	v_mul_f32_e32 v16, v61, v159
	v_fmac_f32_e32 v47, v19, v16
	v_cvt_pk_bf16_f32 v48, v47, s0
	global_load_dwordx4 v[16:19], v158, s[8:9] offset:2288
	global_load_dwordx4 v[44:47], v158, s[10:11] offset:2288
	ds_write_b16 v162, v48 offset:12784
	v_lshlrev_b32_e32 v48, 16, v20
	v_and_b32_e32 v20, 0xffff0000, v20
	v_fmac_f32_e32 v20, 0xbb000000, v157
	v_mul_f32_e32 v20, v20, v159
	v_lshlrev_b32_e32 v49, 16, v21
	v_fmac_f32_e32 v49, 0xbb000000, v157
	v_and_b32_e32 v21, 0xffff0000, v21
	v_fmac_f32_e32 v21, 0xbb000000, v157
	v_lshlrev_b32_e32 v50, 16, v22
	v_fmac_f32_e32 v50, 0xbb000000, v157
	v_and_b32_e32 v22, 0xffff0000, v22
	v_fmac_f32_e32 v22, 0xbb000000, v157
	v_lshlrev_b32_e32 v51, 16, v23
	v_fmac_f32_e32 v51, 0xbb000000, v157
	v_and_b32_e32 v23, 0xffff0000, v23
	s_waitcnt vmcnt(6)
	v_fma_f32 v20, v33, v20, v53
	v_cvt_pk_bf16_f32 v20, v20, s0
	ds_write_b16 v162, v20 offset:13328
	v_mul_f32_e32 v20, v49, v159
	v_fma_f32 v20, v34, v20, v54
	v_cvt_pk_bf16_f32 v20, v20, s0
	ds_write_b16 v162, v20 offset:13600
	v_mul_f32_e32 v20, v21, v159
	v_fmac_f32_e32 v55, v35, v20
	v_cvt_pk_bf16_f32 v20, v55, s0
	ds_write_b16 v162, v20 offset:13872
	v_mul_f32_e32 v20, v50, v159
	v_fmac_f32_e32 v23, 0xbb000000, v157
	v_lshlrev_b32_e32 v21, 16, v13
	s_waitcnt vmcnt(4)
	v_fma_f32 v20, v28, v20, v40
	v_cvt_pk_bf16_f32 v20, v20, s0
	ds_write_b16 v162, v20 offset:14144
	v_mul_f32_e32 v20, v22, v159
	v_fma_f32 v20, v29, v20, v41
	v_cvt_pk_bf16_f32 v20, v20, s0
	ds_write_b16 v162, v20 offset:14416
	v_mul_f32_e32 v20, v51, v159
	v_fma_f32 v20, v30, v20, v42
	v_cvt_pk_bf16_f32 v20, v20, s0
	ds_write_b16 v162, v20 offset:14688
	v_mul_f32_e32 v20, v23, v159
	v_fmac_f32_e32 v43, v31, v20
	v_cvt_pk_bf16_f32 v20, v43, s0
	ds_write_b16 v162, v20 offset:14960
	v_lshlrev_b32_e32 v20, 16, v12
	v_and_b32_e32 v12, 0xffff0000, v12
	v_fmac_f32_e32 v12, 0xbb000000, v157
	v_mul_f32_e32 v12, v12, v159
	v_fmac_f32_e32 v21, 0xbb000000, v157
	v_and_b32_e32 v13, 0xffff0000, v13
	v_fmac_f32_e32 v13, 0xbb000000, v157
	v_lshlrev_b32_e32 v22, 16, v14
	v_fmac_f32_e32 v22, 0xbb000000, v157
	v_and_b32_e32 v14, 0xffff0000, v14
	v_fmac_f32_e32 v14, 0xbb000000, v157
	v_lshlrev_b32_e32 v23, 16, v15
	v_fmac_f32_e32 v23, 0xbb000000, v157
	v_and_b32_e32 v15, 0xffff0000, v15
	v_fmac_f32_e32 v15, 0xbb000000, v157
	v_fmac_f32_e32 v48, 0xbb000000, v157
	v_fmac_f32_e32 v20, 0xbb000000, v157
	v_mul_f32_e32 v48, v48, v159
	s_waitcnt vmcnt(2)
	v_fma_f32 v12, v25, v12, v37
	v_cvt_pk_bf16_f32 v12, v12, s0
	ds_write_b16 v162, v12 offset:15504
	v_mul_f32_e32 v12, v21, v159
	v_fma_f32 v12, v26, v12, v38
	v_cvt_pk_bf16_f32 v12, v12, s0
	ds_write_b16 v162, v12 offset:15776
	v_mul_f32_e32 v12, v13, v159
	v_fmac_f32_e32 v39, v27, v12
	v_cvt_pk_bf16_f32 v12, v39, s0
	ds_write_b16 v162, v12 offset:16048
	v_mul_f32_e32 v12, v22, v159
	v_mul_f32_e32 v20, v20, v159
	v_fma_f32 v32, v32, v48, v52
	v_fma_f32 v20, v24, v20, v36
	v_cvt_pk_bf16_f32 v32, v32, s0
	s_waitcnt vmcnt(0)
	v_fma_f32 v12, v16, v12, v44
	v_cvt_pk_bf16_f32 v12, v12, s0
	ds_write_b16 v162, v12 offset:16320
	v_mul_f32_e32 v12, v14, v159
	v_fma_f32 v12, v17, v12, v45
	v_cvt_pk_bf16_f32 v12, v12, s0
	ds_write_b16 v162, v12 offset:16592
	v_mul_f32_e32 v12, v23, v159
	v_fma_f32 v12, v18, v12, v46
	v_cvt_pk_bf16_f32 v12, v12, s0
	ds_write_b16 v162, v12 offset:16864
	v_mul_f32_e32 v12, v15, v159
	v_fmac_f32_e32 v47, v19, v12
	v_cvt_pk_bf16_f32 v12, v47, s0
	ds_write_b16 v162, v12 offset:17136
	v_lshl_or_b32 v12, s34, 6, v161
	v_cvt_pk_bf16_f32 v20, v20, s0
	v_mul_lo_u32 v12, v12, s6
	ds_write_b16 v162, v32 offset:13056
	ds_write_b16 v162, v20 offset:15232
	v_add3_u32 v162, 0, v156, v12
	s_waitcnt lgkmcnt(0)
	s_barrier
; #define LAS __attribute__((address_space(3)))
; __device__ __forceinline__ unsigned pk2(float lo, float hi) { f32x2 v = {lo, hi}; bf16x2_t b = __builtin_convertvector(v, bf16x2_t); return __builtin_bit_cast(unsigned, b); }
; __device__ __forceinline__ float bflo(unsigned w) { return __uint_as_float(w << 16); }
; __device__ __forceinline__ float bfhi(unsigned w) { return __uint_as_float(w & 0xffff0000u); }
; #define MFMA32(a, b, c) __builtin_amdgcn_mfma_f32_32x32x16_bf16((a), (b), (c), 0, 0, 0)
; __device__ __forceinline__ void gmlp_unit(Ctx& C, int l, int uidx) {
;     ...
;     for (int s = 0; s < 8; ++s) {
;         bf16x8 Vf[2];
; #pragma unroll
;         for (int cb = 0; cb < 2; ++cb) Vf[cb] = *(const LAS bf16x8*)(C.lds + (64 * gl + 32 * cb + r32) * VS + (16 * s + 8 * h) * 2);
; #pragma unroll
;         for (int cb = 0; cb < 2; ++cb)
; #pragma unroll
;             for (int pb = 0; pb < 2; ++pb) acc[cb][pb] = MFMA32(Vf[cb], Wf[pb][s], acc[cb][pb]);
;     }
;     bf16* Y = WSP(bf16, WS_YCAT);
; #pragma unroll
;     for (int pb = 0; pb < 2; ++pb) { const int p = 64 * ph + 32 * pb + r32; const float bs = INP(I_GBS)[(l * 8 + g) * 128 + p];
;         bf16* yp = Y + (size_t)(row0 + p) * DM + 1536 + 64 * g + 4 * h;
; #pragma unroll
;         for (int cb = 0; cb < 2; ++cb)
; #pragma unroll
;             for (int rg = 0; rg < 4; ++rg) { const u32x2 uv = upre[pb][cb][rg];
;                 u32x2 w; w.x = pk2(bflo(uv.x) * (acc[cb][pb][4 * rg] + bs), bfhi(uv.x) * (acc[cb][pb][4 * rg + 1] + bs)); w.y = pk2(bflo(uv.y) * (acc[cb][pb][4 * rg + 2] + bs), bfhi(uv.y) * (acc[cb][pb][4 * rg + 3] + bs));
;                 *(u32x2*)(yp + 32 * cb + 8 * rg) = w; } }
	ds_read_b128 v[12:15], v162
	ds_read_b128 v[156:159], v162 offset:32
	s_waitcnt lgkmcnt(1)
	v_mfma_f32_32x32x16_bf16 v[52:67], v[12:15], v[4:7], 0
	s_lshl_b32 s6, s52, 7
	v_mfma_f32_32x32x16_bf16 v[20:35], v[12:15], v[8:11], 0
	ds_read_b128 v[12:15], v162 offset:8704
	ds_read_b128 v[174:177], v162 offset:8736
	s_waitcnt lgkmcnt(1)
	v_mfma_f32_32x32x16_bf16 v[36:51], v[12:15], v[4:7], 0
	v_mfma_f32_32x32x16_bf16 v[4:19], v[12:15], v[8:11], 0
	v_mfma_f32_32x32x16_bf16 v[52:67], v[156:159], v[116:119], v[52:67]
	v_mfma_f32_32x32x16_bf16 v[20:35], v[156:159], v[120:123], v[20:35]
	s_waitcnt lgkmcnt(0)
	v_mfma_f32_32x32x16_bf16 v[36:51], v[174:177], v[116:119], v[36:51]
	v_mfma_f32_32x32x16_bf16 v[4:19], v[174:177], v[120:123], v[4:19]
	ds_read_b128 v[116:119], v162 offset:64
	ds_read_b128 v[120:123], v162 offset:96
	s_waitcnt lgkmcnt(1)
	v_mfma_f32_32x32x16_bf16 v[52:67], v[116:119], v[104:107], v[52:67]
	v_mfma_f32_32x32x16_bf16 v[20:35], v[116:119], v[112:115], v[20:35]
	ds_read_b128 v[116:119], v162 offset:8768
	ds_read_b128 v[156:159], v162 offset:8800
	s_waitcnt lgkmcnt(1)
	v_mfma_f32_32x32x16_bf16 v[36:51], v[116:119], v[104:107], v[36:51]
	v_mfma_f32_32x32x16_bf16 v[4:19], v[116:119], v[112:115], v[4:19]
	v_mfma_f32_32x32x16_bf16 v[52:67], v[120:123], v[100:103], v[52:67]
	v_mfma_f32_32x32x16_bf16 v[20:35], v[120:123], v[108:111], v[20:35]
	s_waitcnt lgkmcnt(0)
	v_mfma_f32_32x32x16_bf16 v[36:51], v[156:159], v[100:103], v[36:51]
	ds_read_b128 v[100:103], v162 offset:128
	ds_read_b128 v[104:107], v162 offset:160
	v_mfma_f32_32x32x16_bf16 v[4:19], v[156:159], v[108:111], v[4:19]
	s_waitcnt lgkmcnt(1)
	v_mfma_f32_32x32x16_bf16 v[52:67], v[100:103], v[88:91], v[52:67]
	v_mfma_f32_32x32x16_bf16 v[20:35], v[100:103], v[96:99], v[20:35]
	ds_read_b128 v[100:103], v162 offset:8832
	ds_read_b128 v[108:111], v162 offset:8864
	s_waitcnt lgkmcnt(1)
	v_mfma_f32_32x32x16_bf16 v[36:51], v[100:103], v[88:91], v[36:51]
	v_mfma_f32_32x32x16_bf16 v[4:19], v[100:103], v[96:99], v[4:19]
	v_mfma_f32_32x32x16_bf16 v[52:67], v[104:107], v[84:87], v[52:67]
	v_mfma_f32_32x32x16_bf16 v[20:35], v[104:107], v[92:95], v[20:35]
	s_waitcnt lgkmcnt(0)
	v_mfma_f32_32x32x16_bf16 v[36:51], v[108:111], v[84:87], v[36:51]
	ds_read_b128 v[84:87], v162 offset:192
	ds_read_b128 v[88:91], v162 offset:224
	v_mfma_f32_32x32x16_bf16 v[4:19], v[108:111], v[92:95], v[4:19]
	s_waitcnt lgkmcnt(1)
	v_mfma_f32_32x32x16_bf16 v[52:67], v[84:87], v[76:79], v[52:67]
	v_mfma_f32_32x32x16_bf16 v[20:35], v[84:87], v[80:83], v[20:35]
	ds_read_b128 v[84:87], v162 offset:8896
	ds_read_b128 v[92:95], v162 offset:8928
	s_waitcnt lgkmcnt(1)
	v_mfma_f32_32x32x16_bf16 v[4:19], v[84:87], v[80:83], v[4:19]
	v_or_b32_e32 v80, s18, v161
	v_lshlrev_b32_e32 v82, 16, v154
	v_and_b32_e32 v83, 0xffff0000, v154
	v_mfma_f32_32x32x16_bf16 v[36:51], v[84:87], v[76:79], v[36:51]
	v_or_b32_e32 v76, s6, v80
	v_ashrrev_i32_e32 v77, 31, v76
	v_lshl_add_u64 v[78:79], v[76:77], 2, s[54:55]
	global_load_dword v244, v[78:79], off offset:128
	global_load_dword v78, v[78:79], off
	s_ashr_i32 s6, s6, 31
	v_mov_b32_e32 v77, s6
	v_mfma_f32_32x32x16_bf16 v[52:67], v[88:91], v[72:75], v[52:67]
	s_waitcnt lgkmcnt(0)
	v_mfma_f32_32x32x16_bf16 v[36:51], v[92:95], v[72:75], v[36:51]
	v_or_b32_e32 v72, s19, v80
	v_lshlrev_b32_e32 v72, 12, v72
	v_mov_b32_e32 v73, v3
	v_lshl_add_u64 v[74:75], s[46:47], 0, v[72:73]
	v_lshl_add_u64 v[74:75], v[74:75], 0, s[50:51]
	v_lshl_add_u64 v[74:75], v[74:75], 0, v[2:3]
	v_lshl_add_u64 v[80:81], v[74:75], 0, s[36:37]
	v_mfma_f32_32x32x16_bf16 v[20:35], v[88:91], v[68:71], v[20:35]
	s_waitcnt vmcnt(0)
	s_nop 0
	v_add_f32_e64 v52, v52, v78
	v_add_f32_e64 v53, v53, v78
	v_mul_f32_e64 v52, v52, v82
	v_mul_f32_e64 v53, v53, v83
	v_lshlrev_b32_e32 v82, 16, v155
	v_and_b32_e32 v83, 0xffff0000, v155
	v_pk_add_f32 v[54:55], v[54:55], v[78:79] op_sel_hi:[1,0]
	v_cvt_pk_bf16_f32 v52, v52, v53
	v_pk_mul_f32 v[54:55], v[54:55], v[82:83]
	v_pk_add_f32 v[36:37], v[36:37], v[78:79] op_sel_hi:[1,0]
	v_cvt_pk_bf16_f32 v53, v54, v55
	v_add_co_u32_e32 v54, vcc, s69, v74
	v_pk_add_f32 v[38:39], v[38:39], v[78:79] op_sel_hi:[1,0]
	s_nop 0
	v_addc_co_u32_e32 v55, vcc, 0, v75, vcc
	global_store_dwordx2 v[54:55], v[52:53], off offset:3072
	v_lshlrev_b32_e32 v52, 16, v152
	v_and_b32_e32 v53, 0xffff0000, v152
	v_pk_add_f32 v[54:55], v[56:57], v[78:79] op_sel_hi:[1,0]
	v_pk_add_f32 v[56:57], v[58:59], v[78:79] op_sel_hi:[1,0]
	v_pk_mul_f32 v[52:53], v[54:55], v[52:53]
	v_lshlrev_b32_e32 v54, 16, v153
	v_and_b32_e32 v55, 0xffff0000, v153
	v_pk_mul_f32 v[54:55], v[56:57], v[54:55]
	v_cvt_pk_bf16_f32 v52, v52, v53
	v_cvt_pk_bf16_f32 v53, v54, v55
	global_store_dwordx2 v[80:81], v[52:53], off offset:16
	v_lshlrev_b32_e32 v52, 16, v150
	v_and_b32_e32 v53, 0xffff0000, v150
	v_pk_add_f32 v[54:55], v[60:61], v[78:79] op_sel_hi:[1,0]
	v_pk_add_f32 v[56:57], v[62:63], v[78:79] op_sel_hi:[1,0]
	v_pk_mul_f32 v[52:53], v[54:55], v[52:53]
	v_lshlrev_b32_e32 v54, 16, v151
	v_and_b32_e32 v55, 0xffff0000, v151
	v_pk_mul_f32 v[54:55], v[56:57], v[54:55]
	v_cvt_pk_bf16_f32 v52, v52, v53
	v_cvt_pk_bf16_f32 v53, v54, v55
	global_store_dwordx2 v[80:81], v[52:53], off offset:32
	v_lshlrev_b32_e32 v52, 16, v148
	v_and_b32_e32 v53, 0xffff0000, v148
	v_pk_add_f32 v[54:55], v[64:65], v[78:79] op_sel_hi:[1,0]
	v_pk_add_f32 v[56:57], v[66:67], v[78:79] op_sel_hi:[1,0]
	v_pk_mul_f32 v[52:53], v[54:55], v[52:53]
	v_lshlrev_b32_e32 v54, 16, v149
	v_and_b32_e32 v55, 0xffff0000, v149
	v_pk_mul_f32 v[54:55], v[56:57], v[54:55]
	v_cvt_pk_bf16_f32 v52, v52, v53
	v_cvt_pk_bf16_f32 v53, v54, v55
	global_store_dwordx2 v[80:81], v[52:53], off offset:48
; __device__ __forceinline__ unsigned pk2(float lo, float hi) { f32x2 v = {lo, hi}; bf16x2_t b = __builtin_convertvector(v, bf16x2_t); return __builtin_bit_cast(unsigned, b); }
; __device__ __forceinline__ float bflo(unsigned w) { return __uint_as_float(w << 16); }
; __device__ __forceinline__ float bfhi(unsigned w) { return __uint_as_float(w & 0xffff0000u); }
; __device__ __forceinline__ void gmlp_unit(Ctx& C, int l, int uidx) {
;     ...
;     for (int pb = 0; pb < 2; ++pb) { const int p = 64 * ph + 32 * pb + r32; const float bs = INP(I_GBS)[(l * 8 + g) * 128 + p];
;         bf16* yp = Y + (size_t)(row0 + p) * DM + 1536 + 64 * g + 4 * h;
; #pragma unroll
;         for (int cb = 0; cb < 2; ++cb)
; #pragma unroll
;             for (int rg = 0; rg < 4; ++rg) { const u32x2 uv = upre[pb][cb][rg];
;                 u32x2 w; w.x = pk2(bflo(uv.x) * (acc[cb][pb][4 * rg] + bs), bfhi(uv.x) * (acc[cb][pb][4 * rg + 1] + bs)); w.y = pk2(bflo(uv.y) * (acc[cb][pb][4 * rg + 2] + bs), bfhi(uv.y) * (acc[cb][pb][4 * rg + 3] + bs));
;                 *(u32x2*)(yp + 32 * cb + 8 * rg) = w; } }
	v_lshlrev_b32_e32 v52, 16, v146
	v_and_b32_e32 v53, 0xffff0000, v146
	v_pk_mul_f32 v[36:37], v[36:37], v[52:53]
	v_lshlrev_b32_e32 v52, 16, v147
	v_and_b32_e32 v53, 0xffff0000, v147
	v_pk_mul_f32 v[38:39], v[38:39], v[52:53]
	v_cvt_pk_bf16_f32 v36, v36, v37
	v_cvt_pk_bf16_f32 v37, v38, v39
	global_store_dwordx2 v[80:81], v[36:37], off offset:64
	v_lshlrev_b32_e32 v36, 16, v144
	v_and_b32_e32 v37, 0xffff0000, v144
	v_pk_add_f32 v[38:39], v[40:41], v[78:79] op_sel_hi:[1,0]
	v_pk_add_f32 v[40:41], v[42:43], v[78:79] op_sel_hi:[1,0]
	v_pk_mul_f32 v[36:37], v[38:39], v[36:37]
	v_lshlrev_b32_e32 v38, 16, v145
	v_and_b32_e32 v39, 0xffff0000, v145
	v_pk_mul_f32 v[38:39], v[40:41], v[38:39]
	v_cvt_pk_bf16_f32 v36, v36, v37
	v_cvt_pk_bf16_f32 v37, v38, v39
	global_store_dwordx2 v[80:81], v[36:37], off offset:80
	v_lshlrev_b32_e32 v36, 16, v142
	v_and_b32_e32 v37, 0xffff0000, v142
	v_pk_add_f32 v[38:39], v[44:45], v[78:79] op_sel_hi:[1,0]
	v_pk_add_f32 v[40:41], v[46:47], v[78:79] op_sel_hi:[1,0]
	v_pk_mul_f32 v[36:37], v[38:39], v[36:37]
	v_lshlrev_b32_e32 v38, 16, v143
	v_and_b32_e32 v39, 0xffff0000, v143
	v_pk_mul_f32 v[38:39], v[40:41], v[38:39]
	v_cvt_pk_bf16_f32 v36, v36, v37
	v_cvt_pk_bf16_f32 v37, v38, v39
	global_store_dwordx2 v[80:81], v[36:37], off offset:96
	v_lshlrev_b32_e32 v36, 16, v140
	v_and_b32_e32 v37, 0xffff0000, v140
	v_pk_add_f32 v[38:39], v[48:49], v[78:79] op_sel_hi:[1,0]
	v_pk_add_f32 v[40:41], v[50:51], v[78:79] op_sel_hi:[1,0]
	v_pk_mul_f32 v[36:37], v[38:39], v[36:37]
	v_lshlrev_b32_e32 v38, 16, v141
	v_and_b32_e32 v39, 0xffff0000, v141
	v_pk_mul_f32 v[38:39], v[40:41], v[38:39]
	v_cvt_pk_bf16_f32 v36, v36, v37
	v_cvt_pk_bf16_f32 v37, v38, v39
	global_store_dwordx2 v[80:81], v[36:37], off offset:112
	v_mov_b32_e32 v36, v244
	v_or_b32_e32 v38, 0x20000, v72
	v_mov_b32_e32 v39, v3
	v_lshl_add_u64 v[38:39], s[46:47], 0, v[38:39]
	v_lshlrev_b32_e32 v42, 16, v138
	v_and_b32_e32 v43, 0xffff0000, v138
	v_lshl_add_u64 v[38:39], v[38:39], 0, s[50:51]
	v_lshl_add_u64 v[38:39], v[38:39], 0, v[2:3]
	v_lshl_add_u64 v[40:41], v[38:39], 0, s[36:37]
	v_mfma_f32_32x32x16_bf16 v[4:19], v[92:95], v[68:71], v[4:19]
	v_add_f32_e64 v20, v20, v36
	v_add_f32_e64 v21, v21, v36
	v_mul_f32_e64 v20, v20, v42
	v_mul_f32_e64 v21, v21, v43
	v_lshlrev_b32_e32 v42, 16, v139
	v_and_b32_e32 v43, 0xffff0000, v139
	v_pk_add_f32 v[22:23], v[22:23], v[36:37] op_sel_hi:[1,0]
	v_cvt_pk_bf16_f32 v20, v20, v21
	v_pk_mul_f32 v[22:23], v[22:23], v[42:43]
	s_nop 1
	v_pk_add_f32 v[4:5], v[4:5], v[36:37] op_sel_hi:[1,0]
	v_cvt_pk_bf16_f32 v21, v22, v23
	v_add_co_u32_e32 v22, vcc, s69, v38
	v_pk_add_f32 v[6:7], v[6:7], v[36:37] op_sel_hi:[1,0]
	s_nop 0
	v_addc_co_u32_e32 v23, vcc, 0, v39, vcc
	global_store_dwordx2 v[22:23], v[20:21], off offset:3072
	v_lshlrev_b32_e32 v20, 16, v136
	v_and_b32_e32 v21, 0xffff0000, v136
	v_pk_add_f32 v[22:23], v[24:25], v[36:37] op_sel_hi:[1,0]
	v_pk_add_f32 v[24:25], v[26:27], v[36:37] op_sel_hi:[1,0]
	v_pk_mul_f32 v[20:21], v[22:23], v[20:21]
	v_lshlrev_b32_e32 v22, 16, v137
	v_and_b32_e32 v23, 0xffff0000, v137
	v_pk_mul_f32 v[22:23], v[24:25], v[22:23]
	v_cvt_pk_bf16_f32 v20, v20, v21
	v_cvt_pk_bf16_f32 v21, v22, v23
	global_store_dwordx2 v[40:41], v[20:21], off offset:16
	v_lshlrev_b32_e32 v20, 16, v134
	v_and_b32_e32 v21, 0xffff0000, v134
	v_pk_add_f32 v[22:23], v[28:29], v[36:37] op_sel_hi:[1,0]
	v_pk_add_f32 v[24:25], v[30:31], v[36:37] op_sel_hi:[1,0]
	v_pk_mul_f32 v[20:21], v[22:23], v[20:21]
	v_lshlrev_b32_e32 v22, 16, v135
	v_and_b32_e32 v23, 0xffff0000, v135
	v_pk_mul_f32 v[22:23], v[24:25], v[22:23]
	v_cvt_pk_bf16_f32 v20, v20, v21
	v_cvt_pk_bf16_f32 v21, v22, v23
	global_store_dwordx2 v[40:41], v[20:21], off offset:32
	v_lshlrev_b32_e32 v20, 16, v132
	v_and_b32_e32 v21, 0xffff0000, v132
	v_pk_add_f32 v[22:23], v[32:33], v[36:37] op_sel_hi:[1,0]
	v_pk_add_f32 v[24:25], v[34:35], v[36:37] op_sel_hi:[1,0]
	v_pk_mul_f32 v[20:21], v[22:23], v[20:21]
	v_lshlrev_b32_e32 v22, 16, v133
	v_and_b32_e32 v23, 0xffff0000, v133
	v_pk_mul_f32 v[22:23], v[24:25], v[22:23]
	v_cvt_pk_bf16_f32 v20, v20, v21
	v_cvt_pk_bf16_f32 v21, v22, v23
	global_store_dwordx2 v[40:41], v[20:21], off offset:48
	v_lshlrev_b32_e32 v20, 16, v130
	v_and_b32_e32 v21, 0xffff0000, v130
	v_pk_mul_f32 v[4:5], v[4:5], v[20:21]
	v_lshlrev_b32_e32 v20, 16, v131
	v_and_b32_e32 v21, 0xffff0000, v131
	v_pk_mul_f32 v[6:7], v[6:7], v[20:21]
	v_cvt_pk_bf16_f32 v4, v4, v5
	v_cvt_pk_bf16_f32 v5, v6, v7
	global_store_dwordx2 v[40:41], v[4:5], off offset:64
	v_lshlrev_b32_e32 v4, 16, v128
	v_and_b32_e32 v5, 0xffff0000, v128
	v_pk_add_f32 v[6:7], v[8:9], v[36:37] op_sel_hi:[1,0]
	v_pk_add_f32 v[8:9], v[10:11], v[36:37] op_sel_hi:[1,0]
	v_pk_mul_f32 v[4:5], v[6:7], v[4:5]
	v_lshlrev_b32_e32 v6, 16, v129
	v_and_b32_e32 v7, 0xffff0000, v129
	v_pk_mul_f32 v[6:7], v[8:9], v[6:7]
	v_cvt_pk_bf16_f32 v4, v4, v5
	v_cvt_pk_bf16_f32 v5, v6, v7
	global_store_dwordx2 v[40:41], v[4:5], off offset:80
	v_lshlrev_b32_e32 v4, 16, v126
	v_and_b32_e32 v5, 0xffff0000, v126
	v_pk_add_f32 v[6:7], v[12:13], v[36:37] op_sel_hi:[1,0]
	v_pk_add_f32 v[8:9], v[14:15], v[36:37] op_sel_hi:[1,0]
	v_pk_mul_f32 v[4:5], v[6:7], v[4:5]
	v_lshlrev_b32_e32 v6, 16, v127
	v_and_b32_e32 v7, 0xffff0000, v127
	v_pk_mul_f32 v[6:7], v[8:9], v[6:7]
	v_cvt_pk_bf16_f32 v4, v4, v5
	v_cvt_pk_bf16_f32 v5, v6, v7
	global_store_dwordx2 v[40:41], v[4:5], off offset:96
	v_lshlrev_b32_e32 v4, 16, v124
	v_and_b32_e32 v5, 0xffff0000, v124
	v_pk_add_f32 v[6:7], v[16:17], v[36:37] op_sel_hi:[1,0]
	v_pk_add_f32 v[8:9], v[18:19], v[36:37] op_sel_hi:[1,0]
	v_pk_mul_f32 v[4:5], v[6:7], v[4:5]
	v_lshlrev_b32_e32 v6, 16, v125
	v_and_b32_e32 v7, 0xffff0000, v125
	v_pk_mul_f32 v[6:7], v[8:9], v[6:7]
	v_cvt_pk_bf16_f32 v4, v4, v5
	v_cvt_pk_bf16_f32 v5, v6, v7
	global_store_dwordx2 v[40:41], v[4:5], off offset:112
